# k8: + P9 b1 prefetch into free VGPRs, re-stagger barrier moved before K-loop in P9 and P10
# speedup vs baseline: 1.0177x; 1.0023x over previous
;     __device__ __forceinline__ bool next(int i, Unit& u) const { const int L = i * G + c; if (L >= nunits) return false; u.e = L / nPM; u.pm = L % nPM; u.pn = 0; u.rb = 0; u.nvalid = 256; return true; }
;     __device__ __forceinline__ bool next(int i, Unit& u) const {
;         const int L = i * G + c; const int total = (int)M[176]; if (L >= total) return false;
;         const int ln = threadIdx.x & 63; const int us1 = (int)M[33 + (ln & 31)];
;         const int e = __builtin_popcountll(__ballot(ln < 32 && L >= us1));
;         const int w = L - (int)M[32 + e], pb = (int)M[80 + e], nb = (int)M[80 + e + 1] - pb, cnt = (int)M[128 + e];
;         int rb = w % nb, pn = w / nb;
;         rb = __builtin_amdgcn_readfirstlane(rb); pn = __builtin_amdgcn_readfirstlane(pn);
;         u.e = e; u.rb = rb; u.pn = pn; u.pm = __builtin_amdgcn_readfirstlane(pb + rb); const int nv = cnt - rb * 256; u.nvalid = __builtin_amdgcn_readfirstlane(nv < 256 ? nv : 256); return true;
;     }
;     __device__ __forceinline__ void operator()(EPI_ARGS) const {
;         const int j0 = u.pn * 128 + wc * 32 + 8 * fq; const float* bb = b1 + (size_t)u.e * 2 * FE;
;         const f32x4 ba0 = *(const f32x4*)(bb + j0), ba1 = *(const f32x4*)(bb + j0 + 4), bl0 = *(const f32x4*)(bb + FE + j0), bl1 = *(const f32x4*)(bb + FE + j0 + 4);
.LBB0_1303:
	s_lshl_b32 s8, s30, 7
	s_ashr_i32 s29, s28, 31
	s_or_b32 s8, s8, s69
	v_or_b32_e32 v248, s8, v205
	s_lshl_b64 s[8:9], s[28:29], 14
	s_add_u32 s8, s12, s8
	s_addc_u32 s9, s13, s9
	v_ashrrev_i32_e32 v249, 31, v248
	v_lshl_add_u64 v[248:249], v[248:249], 2, s[8:9]
	v_lshl_add_u64 v[252:253], v[248:249], 0, s[20:21]
	global_load_dwordx4 v[240:243], v[248:249], off
	global_load_dwordx4 v[244:247], v[248:249], off offset:16
	global_load_dwordx4 v[248:251], v[252:253], off
	global_load_dword v255, v[252:253], off offset:24
	global_load_dword v239, v[252:253], off offset:28
	global_load_dwordx2 v[252:253], v[252:253], off offset:16
	ds_read_b32 v2, v222
	s_add_i32 s67, s67, 1
	s_mul_i32 s6, s67, s50
	s_add_i32 s6, s6, s51
	s_waitcnt lgkmcnt(0)
	v_readfirstlane_b32 s7, v2
	v_cmp_ge_i32_e32 vcc, s6, v2
	s_cmp_lt_i32 s6, s7
	s_cselect_b64 s[40:41], -1, 0
	s_cbranch_vccnz .LBB0_1305
	ds_read_b32 v2, v221 offset:132
	s_waitcnt lgkmcnt(0)
	v_cmp_ge_i32_e32 vcc, s6, v2
	s_and_b64 s[8:9], s[4:5], vcc
	v_cndmask_b32_e64 v2, 0, 1, s[8:9]
	v_cmp_ne_u32_e32 vcc, 0, v2
	s_bcnt1_i32_b64 s22, vcc
	s_lshl_b32 s7, s22, 2
	s_add_i32 s7, s7, 0
	s_add_i32 s7, s7, 0x20140
	v_mov_b32_e32 v2, s7
	ds_read_b32 v3, v2 offset:128
	ds_read_b32 v4, v2 offset:320
	ds_read_b32 v5, v2 offset:324
	ds_read_b32 v2, v2 offset:512
	s_waitcnt lgkmcnt(0)
	v_readfirstlane_b32 s11, v3
	v_readfirstlane_b32 s8, v4
	v_readfirstlane_b32 s7, v5
	s_sub_i32 s7, s7, s8
	s_abs_i32 s9, s7
	v_cvt_f32_u32_e32 v4, s9
	s_sub_i32 s15, 0, s9
	s_sub_i32 s6, s6, s11
	s_abs_i32 s14, s6
	v_rcp_iflag_f32_e32 v4, v4
	s_xor_b32 s11, s6, s7
	s_ashr_i32 s11, s11, 31
	v_mul_f32_e32 v3, 0x4f7ffffe, v4
	v_cvt_u32_f32_e32 v3, v3
	s_nop 0
	v_readfirstlane_b32 s23, v3
	s_mul_i32 s15, s15, s23
	s_mul_hi_u32 s15, s23, s15
	s_add_i32 s23, s23, s15
	s_mul_hi_u32 s15, s14, s23
	s_mul_i32 s23, s15, s9
	s_sub_i32 s14, s14, s23
	s_add_i32 s24, s15, 1
	s_sub_i32 s23, s14, s9
	s_cmp_ge_u32 s14, s9
	s_cselect_b32 s15, s24, s15
	s_cselect_b32 s14, s23, s14
	s_add_i32 s23, s15, 1
	s_cmp_ge_u32 s14, s9
	s_cselect_b32 s9, s23, s15
	s_xor_b32 s9, s9, s11
	s_sub_i32 s24, s9, s11
	s_mul_i32 s7, s24, s7
	s_sub_i32 s78, s6, s7
	s_lshl_b32 s6, s78, 8
	v_subrev_u32_e32 v2, s6, v2
	v_min_i32_e32 v2, 0x100, v2
	s_add_i32 s80, s8, s78
	v_readfirstlane_b32 s79, v2

; #define PG8_BAR __builtin_amdgcn_s_barrier()
;     __device__ __forceinline__ unsigned a_rowoff(const Unit& u, int r) const { const int idx = (r < u.nvalid) ? (u.rb * 256 + r) : 0; const int tok = ltok[(size_t)u.e * LCAP + idx]; return (unsigned)tok * (unsigned)D; }
;     __device__ __forceinline__ int krot(const Unit& u, int nt) const { return (2 * u.rb + u.pn) % nt; }
;     ...
;         rotn = has_next ? S.krot(nxt, nt) : rotc;
;         const bool full = !HALFU || cur.nvalid > 128;
; #pragma unroll 1
;         for (int t = 0; t < nt; t += 2) {
;             const bool last = (t == nt - 2);
;             const bool fin = last && !has_next;
;             const char* a1 = cA + PG8_KOFS(rotc, t + 1);
;             const size_t k2 = last ? PG8_KOFS(rotn, 0) : PG8_KOFS(rotc, t + 2), k3 = last ? PG8_KOFS(rotn, 1) : PG8_KOFS(rotc, t + 3);
;             const char* a2 = (last ? nA : cA) + k2; const char* b2 = (last ? nB : cB) + k2;
;             const char* a3 = (last ? nA : cA) + k3; const char* b3 = (last ? nB : cB) + k3;
;             unsigned o2[2][2];
; #pragma unroll
;             for (int h = 0; h < 2; ++h)
; #pragma unroll
;                 for (int i = 0; i < 2; ++i) o2[h][i] = gcur[h][i];
;             if constexpr (GATHER) {
;                 if (t == 0 && has_next) {
; #pragma unroll
;                     for (int h = 0; h < 2; ++h)
; #pragma unroll
;                         for (int i = 0; i < 2; ++i) gnxt[h][i] = S.a_rowoff(nxt, h * HALF + rowA[i]) + colA[i];
;                 }
;                 if (last && has_next) {
;                     asm volatile("" : "+v"(gnxt[0][0]), "+v"(gnxt[0][1]), "+v"(gnxt[1][0]), "+v"(gnxt[1][1]));
; #pragma unroll
;                     for (int h = 0; h < 2; ++h)
; #pragma unroll
;                         for (int i = 0; i < 2; ++i) o2[h][i] = gnxt[h][i];
;                 }
;             }
;     ...
; #pragma unroll
;         for (int a = 0; a < 2; ++a)
; #pragma unroll
;             for (int b = 0; b < 2; ++b)
; #pragma unroll
;                 for (int m = 0; m < 4; ++m)
; #pragma unroll
;                     for (int n = 0; n < 2; ++n) acc[a][b][m][n] = (f32x4){0.f, 0.f, 0.f, 0.f};
;         cur = nxt; cA = nA; cB = nB; rotc = rotn; ++ui;
; #pragma unroll
;         for (int h = 0; h < 2; ++h)
; #pragma unroll
;             for (int i = 0; i < 2; ++i) gcur[h][i] = gnxt[h][i];
;         if (wr == 1) PG8_BAR;
.LBB0_1307:
	s_lshl_b32 s8, s78, 1
	s_add_i32 s8, s24, s8
	s_ashr_i32 s9, s8, 31
	s_lshr_b32 s9, s9, 28
	s_add_i32 s9, s8, s9
	s_and_b32 s9, s9, -16
	s_sub_i32 s25, s8, s9
	s_and_b64 s[8:9], s[40:41], exec
	s_cselect_b32 s42, s25, s38
	s_cmpk_gt_i32 s10, 0x80
	s_cselect_b64 s[44:45], -1, 0
	s_ashr_i32 s43, s42, 31
	s_xor_b64 s[46:47], s[40:41], -1
	s_lshl_b64 s[8:9], s[42:43], 7
	s_add_u32 s8, s8, 0x80
	s_addc_u32 s9, s9, 0
	s_cmp_lt_i32 s42, 15
	s_cselect_b32 s29, s9, 0
	s_cselect_b32 s43, s8, 0
	s_lshl_b32 s10, s78, 8
	v_or_b32_e32 v2, s10, v1
	v_cmp_gt_i32_e32 vcc, s79, v1
	v_or_b32_e32 v4, s10, v195
	v_or_b32_e32 v6, s10, v216
	v_cndmask_b32_e32 v2, 0, v2, vcc
	v_cmp_gt_i32_e32 vcc, s79, v195
	s_lshl_b64 s[8:9], s[22:23], 16
	v_or_b32_e32 v8, s10, v217
	v_cndmask_b32_e32 v4, 0, v4, vcc
	v_cmp_gt_i32_e32 vcc, s79, v216
	s_add_u32 s8, s49, s8
	v_mov_b32_e32 v68, v201
	v_cndmask_b32_e32 v6, 0, v6, vcc
	v_cmp_gt_i32_e32 vcc, s79, v217
	v_mov_b32_e32 v69, v201
	v_ashrrev_i32_e32 v3, 31, v2
	v_cndmask_b32_e32 v8, 0, v8, vcc
	v_ashrrev_i32_e32 v5, 31, v4
	v_ashrrev_i32_e32 v7, 31, v6
	v_ashrrev_i32_e32 v9, 31, v8
	s_addc_u32 s9, s58, s9
	v_mov_b32_e32 v66, v201
	v_mov_b32_e32 v67, v201
	v_mov_b32_e32 v130, 0
	v_mov_b64_e32 v[72:73], v[68:69]
	v_mov_b64_e32 v[84:85], v[68:69]
	v_mov_b64_e32 v[88:89], v[68:69]
	v_mov_b64_e32 v[100:101], v[68:69]
	v_mov_b64_e32 v[104:105], v[68:69]
	v_mov_b64_e32 v[116:117], v[68:69]
	v_mov_b64_e32 v[120:121], v[68:69]
	v_mov_b64_e32 v[76:77], v[68:69]
	v_mov_b64_e32 v[80:81], v[68:69]
	v_mov_b64_e32 v[92:93], v[68:69]
	v_mov_b64_e32 v[96:97], v[68:69]
	v_mov_b64_e32 v[108:109], v[68:69]
	v_mov_b64_e32 v[112:113], v[68:69]
	v_mov_b64_e32 v[124:125], v[68:69]
	v_mov_b64_e32 v[128:129], v[68:69]
	v_mov_b32_e32 v203, v201
	v_lshl_add_u64 v[208:209], v[2:3], 2, s[8:9]
	v_lshl_add_u64 v[210:211], v[4:5], 2, s[8:9]
	v_lshl_add_u64 v[212:213], v[6:7], 2, s[8:9]
	v_lshl_add_u64 v[214:215], v[8:9], 2, s[8:9]
	s_mov_b32 s23, -2
	v_mov_b64_e32 v[70:71], v[66:67]
	v_mov_b64_e32 v[82:83], v[66:67]
	v_mov_b64_e32 v[86:87], v[66:67]
	v_mov_b64_e32 v[98:99], v[66:67]
	v_mov_b64_e32 v[102:103], v[66:67]
	v_mov_b64_e32 v[114:115], v[66:67]
	v_mov_b64_e32 v[118:119], v[66:67]
	v_mov_b64_e32 v[74:75], v[66:67]
	v_mov_b64_e32 v[78:79], v[66:67]
	v_mov_b64_e32 v[90:91], v[66:67]
	v_mov_b64_e32 v[94:95], v[66:67]
	v_mov_b64_e32 v[106:107], v[66:67]
	v_mov_b64_e32 v[110:111], v[66:67]
	v_mov_b64_e32 v[122:123], v[66:67]
	v_mov_b64_e32 v[126:127], v[66:67]
	v_mov_b32_e32 v230, v202
	v_mov_b32_e32 v229, v200
	v_mov_b32_e32 v228, v204
	v_mov_b32_e32 v227, v206
	v_mov_b32_e32 v131, v130
	v_mov_b32_e32 v132, v130
	v_mov_b32_e32 v133, v130
	v_mov_b32_e32 v134, v130
	v_mov_b32_e32 v135, v130
	v_mov_b32_e32 v136, v130
	v_mov_b32_e32 v137, v130
	v_mov_b32_e32 v146, v130
	v_mov_b32_e32 v147, v130
	v_mov_b32_e32 v148, v130
	v_mov_b32_e32 v149, v130
	v_mov_b32_e32 v150, v130
	v_mov_b32_e32 v151, v130
	v_mov_b32_e32 v152, v130
	v_mov_b32_e32 v153, v130
	v_mov_b32_e32 v162, v130
	v_mov_b32_e32 v163, v130
	v_mov_b32_e32 v164, v130
	v_mov_b32_e32 v165, v130
	v_mov_b32_e32 v166, v130
	v_mov_b32_e32 v167, v130
	v_mov_b32_e32 v168, v130
	v_mov_b32_e32 v169, v130
	v_mov_b32_e32 v178, v130
	v_mov_b32_e32 v179, v130
	v_mov_b32_e32 v180, v130
	v_mov_b32_e32 v181, v130
	v_mov_b32_e32 v182, v130
	v_mov_b32_e32 v183, v130
	v_mov_b32_e32 v184, v130
	v_mov_b32_e32 v185, v130
	v_mov_b32_e32 v138, v130
	v_mov_b32_e32 v139, v130
	v_mov_b32_e32 v140, v130
	v_mov_b32_e32 v141, v130
	v_mov_b32_e32 v142, v130
	v_mov_b32_e32 v143, v130
	v_mov_b32_e32 v144, v130
	v_mov_b32_e32 v145, v130
	v_mov_b32_e32 v154, v130
	v_mov_b32_e32 v155, v130
	v_mov_b32_e32 v156, v130
	v_mov_b32_e32 v157, v130
	v_mov_b32_e32 v158, v130
	v_mov_b32_e32 v159, v130
	v_mov_b32_e32 v160, v130
	v_mov_b32_e32 v161, v130
	v_mov_b32_e32 v170, v130
	v_mov_b32_e32 v171, v130
	v_mov_b32_e32 v172, v130
	v_mov_b32_e32 v173, v130
	v_mov_b32_e32 v174, v130
	v_mov_b32_e32 v175, v130
	v_mov_b32_e32 v176, v130
	v_mov_b32_e32 v177, v130
	v_mov_b32_e32 v186, v130
	v_mov_b32_e32 v187, v130
	v_mov_b32_e32 v188, v130
	v_mov_b32_e32 v189, v130
	v_mov_b32_e32 v190, v130
	v_mov_b32_e32 v191, v130
	v_mov_b32_e32 v192, v130
	v_mov_b32_e32 v193, v130
	s_cmp_lt_u32 s67, 2
	s_cbranch_scc1 .Lp9_noR
	s_and_b64 vcc, exec, s[2:3]
	s_cbranch_vccz .Lp9_noR
	s_barrier
.Lp9_noR:
	s_and_b64 vcc, exec, s[44:45]
	s_cbranch_vccz .LBB0_1309
	s_and_b64 vcc, exec, s[40:41]
	s_cbranch_vccz .Lp9_nognxt
	global_load_dword v227, v[208:209], off
	global_load_dword v228, v[210:211], off
	global_load_dword v229, v[212:213], off
	global_load_dword v230, v[214:215], off

; #define PG8_STAGE2(bufoff, gbase, o0, o1) do { \
;         __builtin_amdgcn_global_load_lds((const unsigned*)((const char*)(gbase) + (o0)), (PG8_LAS unsigned*)(lds + (bufoff) + ldsw), 16, 0, 0); \
;         __builtin_amdgcn_global_load_lds((const unsigned*)((const char*)(gbase) + (o1)), (PG8_LAS unsigned*)(lds + (bufoff) + ldsw + 8192), 16, 0, 0); } while (0)
; #define PG8_STAGE_B(bufoff, gbase) PG8_STAGE2(bufoff, gbase, voffB[0], voffB[1])
; #define PG8_WAIT_V(n) asm volatile("s_waitcnt vmcnt(" #n ")" ::: "memory")
; #define PG8_WAIT_L(n) asm volatile("s_waitcnt lgkmcnt(" #n ")" ::: "memory")
; #define PG8_BAR __builtin_amdgcn_s_barrier()
; #define PG8_SCHED __builtin_amdgcn_sched_barrier(0)
;     ...
;             PG8_LDB(B0, 0, 0); PG8_LDB(B1, 0, 1); PG8_SCHED; PG8_LDA(At, 0, 0); PG8_STAGE2(PG8_SA(1, 1), a1 + hstepA, gcur[1][0], gcur[1][1]);
;             PG8_WAIT_V(8); PG8_WAIT_L(0); PG8_BAR; PG8_MMA(0, 0, At, B0); PG8_MMA(0, 1, At, B1); PG8_BAR; PG8_SCHED;
;             if (full) { PG8_LDA(At, 0, 1); }
;             if (!fin) { PG8_STAGE_B(PG8_SB(0, 0), b2); PG8_STAGE_B(PG8_SB(0, 1), b2 + hstepB); PG8_STAGE2(PG8_SA(0, 0), a2, o2[0][0], o2[0][1]); PG8_WAIT_V(8); }
;             else { PG8_WAIT_V(2); }
;             PG8_WAIT_L(0); PG8_BAR; if (full) { PG8_MMA(1, 0, At, B0); PG8_MMA(1, 1, At, B1); } PG8_BAR; PG8_SCHED;
.Lp9_top:
	s_add_i32 s82, s38, s23
	s_add_i32 s84, s82, 3
	s_and_b32 s84, s84, 15
	s_lshl_b32 s84, s84, 7
	s_add_u32 s8, s59, s84
	s_addc_u32 s9, s60, 0
	ds_read_b128 v[10:13], v238
	ds_read_b128 v[14:17], v238 offset:1024
	ds_read_b128 v[26:29], v238 offset:2048
	ds_read_b128 v[30:33], v238 offset:3072
	ds_read_b128 v[2:5], v238 offset:16384
	ds_read_b128 v[6:9], v238 offset:17408
	ds_read_b128 v[18:21], v238 offset:18432
	ds_read_b128 v[22:25], v238 offset:19456
	ds_read_b128 v[34:37], v224
	ds_read_b128 v[38:41], v224 offset:1024
	ds_read_b128 v[42:45], v224 offset:2048
	ds_read_b128 v[46:49], v224 offset:3072
	ds_read_b128 v[50:53], v224 offset:4096
	ds_read_b128 v[54:57], v224 offset:5120
	ds_read_b128 v[58:61], v224 offset:6144
	ds_read_b128 v[62:65], v224 offset:7168
	s_add_i32 m0, s31, 0xc000
	s_nop 0
	global_load_lds_dwordx4 v200, s[8:9]
	s_add_i32 m0, s31, 0xe000
	s_nop 0
	global_load_lds_dwordx4 v202, s[8:9]
	s_waitcnt vmcnt(8)
	s_waitcnt lgkmcnt(0)
	s_barrier
	s_setprio 1
	s_nop 1
	v_mfma_f32_16x16x128_f8f6f4 v[190:193], v[10:17], v[34:41], v[190:193]
	v_mfma_f32_16x16x128_f8f6f4 v[186:189], v[26:33], v[34:41], v[186:189]
	v_mfma_f32_16x16x128_f8f6f4 v[174:177], v[10:17], v[42:49], v[174:177]
	v_mfma_f32_16x16x128_f8f6f4 v[170:173], v[26:33], v[42:49], v[170:173]
	v_mfma_f32_16x16x128_f8f6f4 v[158:161], v[10:17], v[50:57], v[158:161]
	v_mfma_f32_16x16x128_f8f6f4 v[154:157], v[26:33], v[50:57], v[154:157]
	v_mfma_f32_16x16x128_f8f6f4 v[142:145], v[10:17], v[58:65], v[142:145]
	v_mfma_f32_16x16x128_f8f6f4 v[138:141], v[26:33], v[58:65], v[138:141]
	v_mfma_f32_16x16x128_f8f6f4 v[182:185], v[2:9], v[34:41], v[182:185]
	v_mfma_f32_16x16x128_f8f6f4 v[178:181], v[18:25], v[34:41], v[178:181]
	v_mfma_f32_16x16x128_f8f6f4 v[166:169], v[2:9], v[42:49], v[166:169]
	v_mfma_f32_16x16x128_f8f6f4 v[162:165], v[18:25], v[42:49], v[162:165]
	v_mfma_f32_16x16x128_f8f6f4 v[150:153], v[2:9], v[50:57], v[150:153]
	v_mfma_f32_16x16x128_f8f6f4 v[146:149], v[18:25], v[50:57], v[146:149]
	v_mfma_f32_16x16x128_f8f6f4 v[134:137], v[2:9], v[58:65], v[134:137]
	v_mfma_f32_16x16x128_f8f6f4 v[130:133], v[18:25], v[58:65], v[130:133]
	s_setprio 0
	s_barrier
	s_add_i32 s84, s82, 4
	s_and_b32 s84, s84, 15
	s_lshl_b32 s84, s84, 7
	ds_read_b128 v[34:37], v224 offset:16384
	ds_read_b128 v[38:41], v224 offset:17408
	ds_read_b128 v[42:45], v224 offset:18432
	ds_read_b128 v[46:49], v224 offset:19456
	ds_read_b128 v[50:53], v224 offset:20480
	ds_read_b128 v[54:57], v224 offset:21504
	ds_read_b128 v[58:61], v224 offset:22528
	ds_read_b128 v[62:65], v224 offset:23552
	s_add_u32 s52, s36, s84
	s_addc_u32 s53, s37, 0
	s_add_u32 s56, s52, 0x40000
	s_addc_u32 s57, s53, 0
	s_add_u32 s14, s59, s84
	s_addc_u32 s15, s60, 0
	s_mov_b32 m0, s39
	s_nop 0
	global_load_lds_dwordx4 v196, s[52:53]
	s_mov_b32 m0, s61
	s_nop 0
	global_load_lds_dwordx4 v198, s[52:53]
	s_mov_b32 m0, s62
	s_nop 0
	global_load_lds_dwordx4 v196, s[56:57]
	s_mov_b32 m0, s63
	s_nop 0
	global_load_lds_dwordx4 v198, s[56:57]
	s_mov_b32 m0, s31
	s_nop 0
	global_load_lds_dwordx4 v206, s[14:15]
	s_mov_b32 m0, s64
	s_nop 0
	global_load_lds_dwordx4 v204, s[14:15]
	s_waitcnt vmcnt(8)
	s_waitcnt lgkmcnt(0)
	s_barrier
	s_setprio 1
	s_nop 1
	v_mfma_f32_16x16x128_f8f6f4 v[126:129], v[10:17], v[34:41], v[126:129]
	v_mfma_f32_16x16x128_f8f6f4 v[122:125], v[26:33], v[34:41], v[122:125]
	v_mfma_f32_16x16x128_f8f6f4 v[110:113], v[10:17], v[42:49], v[110:113]
	v_mfma_f32_16x16x128_f8f6f4 v[106:109], v[26:33], v[42:49], v[106:109]
	v_mfma_f32_16x16x128_f8f6f4 v[94:97], v[10:17], v[50:57], v[94:97]
	v_mfma_f32_16x16x128_f8f6f4 v[90:93], v[26:33], v[50:57], v[90:93]
	v_mfma_f32_16x16x128_f8f6f4 v[78:81], v[10:17], v[58:65], v[78:81]
	v_mfma_f32_16x16x128_f8f6f4 v[74:77], v[26:33], v[58:65], v[74:77]
	v_mfma_f32_16x16x128_f8f6f4 v[118:121], v[2:9], v[34:41], v[118:121]
	v_mfma_f32_16x16x128_f8f6f4 v[114:117], v[18:25], v[34:41], v[114:117]
	v_mfma_f32_16x16x128_f8f6f4 v[102:105], v[2:9], v[42:49], v[102:105]
	v_mfma_f32_16x16x128_f8f6f4 v[98:101], v[18:25], v[42:49], v[98:101]
	v_mfma_f32_16x16x128_f8f6f4 v[86:89], v[2:9], v[50:57], v[86:89]
	v_mfma_f32_16x16x128_f8f6f4 v[82:85], v[18:25], v[50:57], v[82:85]
	v_mfma_f32_16x16x128_f8f6f4 v[70:73], v[2:9], v[58:65], v[70:73]
	v_mfma_f32_16x16x128_f8f6f4 v[66:69], v[18:25], v[58:65], v[66:69]
	s_setprio 0
	s_barrier
; #define PG8_STAGE2(bufoff, gbase, o0, o1) do { \
;         __builtin_amdgcn_global_load_lds((const unsigned*)((const char*)(gbase) + (o0)), (PG8_LAS unsigned*)(lds + (bufoff) + ldsw), 16, 0, 0); \
;         __builtin_amdgcn_global_load_lds((const unsigned*)((const char*)(gbase) + (o1)), (PG8_LAS unsigned*)(lds + (bufoff) + ldsw + 8192), 16, 0, 0); } while (0)
; #define PG8_STAGE_B(bufoff, gbase) PG8_STAGE2(bufoff, gbase, voffB[0], voffB[1])
; #define PG8_WAIT_V(n) asm volatile("s_waitcnt vmcnt(" #n ")" ::: "memory")
; #define PG8_WAIT_L(n) asm volatile("s_waitcnt lgkmcnt(" #n ")" ::: "memory")
; #define PG8_BAR __builtin_amdgcn_s_barrier()
; #define PG8_SCHED __builtin_amdgcn_sched_barrier(0)
;     ...
;             PG8_LDB(B0, 1, 0); PG8_LDB(B1, 1, 1); PG8_SCHED; PG8_LDA(At, 1, 0);
;             if (!fin) { PG8_STAGE2(PG8_SA(0, 1), a2 + hstepA, o2[1][0], o2[1][1]); PG8_WAIT_V(8); } else { PG8_WAIT_V(0); }
;             PG8_WAIT_L(0); PG8_BAR; PG8_MMA(0, 0, At, B0); PG8_MMA(0, 1, At, B1); PG8_BAR; PG8_SCHED;
;             if (full) { PG8_LDA(At, 1, 1); }
;             if (!fin) { PG8_STAGE_B(PG8_SB(1, 0), b3); PG8_STAGE_B(PG8_SB(1, 1), b3 + hstepB); PG8_STAGE2(PG8_SA(1, 0), a3, o2[0][0], o2[0][1]); PG8_WAIT_V(8); }
;             PG8_WAIT_L(0); PG8_BAR; if (full) { PG8_MMA(1, 0, At, B0); PG8_MMA(1, 1, At, B1); } PG8_BAR; PG8_SCHED;
;         }
	s_add_i32 s84, s82, 5
	s_and_b32 s84, s84, 15
	s_lshl_b32 s84, s84, 7
	ds_read_b128 v[50:53], v238 offset:32768
	ds_read_b128 v[54:57], v238 offset:33792
	ds_read_b128 v[58:61], v238 offset:34816
	ds_read_b128 v[62:65], v238 offset:35840
	ds_read_b128 v[2:5], v238 offset:49152
	ds_read_b128 v[6:9], v238 offset:50176
	ds_read_b128 v[10:13], v238 offset:51200
	ds_read_b128 v[14:17], v238 offset:52224
	ds_read_b128 v[18:21], v224 offset:32768
	ds_read_b128 v[22:25], v224 offset:33792
	ds_read_b128 v[26:29], v224 offset:34816
	ds_read_b128 v[30:33], v224 offset:35840
	ds_read_b128 v[34:37], v224 offset:36864
	ds_read_b128 v[38:41], v224 offset:37888
	ds_read_b128 v[42:45], v224 offset:38912
	ds_read_b128 v[46:49], v224 offset:39936
	s_mov_b32 m0, s65
	s_nop 0
	global_load_lds_dwordx4 v200, s[14:15]
	s_mov_b32 m0, s66
	s_nop 0
	global_load_lds_dwordx4 v202, s[14:15]
	s_waitcnt vmcnt(8)
	s_waitcnt lgkmcnt(0)
	s_barrier
	s_setprio 1
	s_nop 1
	v_mfma_f32_16x16x128_f8f6f4 v[190:193], v[50:57], v[18:25], v[190:193]
	v_mfma_f32_16x16x128_f8f6f4 v[186:189], v[58:65], v[18:25], v[186:189]
	v_mfma_f32_16x16x128_f8f6f4 v[174:177], v[50:57], v[26:33], v[174:177]
	v_mfma_f32_16x16x128_f8f6f4 v[170:173], v[58:65], v[26:33], v[170:173]
	v_mfma_f32_16x16x128_f8f6f4 v[158:161], v[50:57], v[34:41], v[158:161]
	v_mfma_f32_16x16x128_f8f6f4 v[154:157], v[58:65], v[34:41], v[154:157]
	v_mfma_f32_16x16x128_f8f6f4 v[142:145], v[50:57], v[42:49], v[142:145]
	v_mfma_f32_16x16x128_f8f6f4 v[138:141], v[58:65], v[42:49], v[138:141]
	v_mfma_f32_16x16x128_f8f6f4 v[182:185], v[2:9], v[18:25], v[182:185]
	v_mfma_f32_16x16x128_f8f6f4 v[178:181], v[10:17], v[18:25], v[178:181]
	v_mfma_f32_16x16x128_f8f6f4 v[166:169], v[2:9], v[26:33], v[166:169]
	v_mfma_f32_16x16x128_f8f6f4 v[162:165], v[10:17], v[26:33], v[162:165]
	v_mfma_f32_16x16x128_f8f6f4 v[150:153], v[2:9], v[34:41], v[150:153]
	v_mfma_f32_16x16x128_f8f6f4 v[146:149], v[10:17], v[34:41], v[146:149]
	v_mfma_f32_16x16x128_f8f6f4 v[134:137], v[2:9], v[42:49], v[134:137]
	v_mfma_f32_16x16x128_f8f6f4 v[130:133], v[10:17], v[42:49], v[130:133]
	s_setprio 0
	s_barrier
	ds_read_b128 v[18:21], v224 offset:49152
	ds_read_b128 v[22:25], v224 offset:50176
	ds_read_b128 v[26:29], v224 offset:51200
	ds_read_b128 v[30:33], v224 offset:52224
	ds_read_b128 v[34:37], v224 offset:53248
	ds_read_b128 v[38:41], v224 offset:54272
	ds_read_b128 v[42:45], v224 offset:55296
	ds_read_b128 v[46:49], v224 offset:56320
	s_add_u32 s10, s36, s84
	s_addc_u32 s11, s37, 0
	s_add_u32 s34, s10, 0x40000
	s_addc_u32 s35, s11, 0
	s_add_u32 s90, s59, s84
	s_addc_u32 s91, s60, 0
	s_mov_b32 m0, s70
	s_nop 0
	global_load_lds_dwordx4 v196, s[10:11]
	s_mov_b32 m0, s71
	s_nop 0
	global_load_lds_dwordx4 v198, s[10:11]
	s_mov_b32 m0, s74
	s_nop 0
	global_load_lds_dwordx4 v196, s[34:35]
	s_mov_b32 m0, s75
	s_nop 0
	global_load_lds_dwordx4 v198, s[34:35]
	s_mov_b32 m0, s72
	s_nop 0
	global_load_lds_dwordx4 v206, s[90:91]
	s_mov_b32 m0, s73
	s_nop 0
	global_load_lds_dwordx4 v204, s[90:91]
	s_waitcnt vmcnt(8)
	s_waitcnt lgkmcnt(0)
	s_barrier
	s_setprio 1
	s_nop 1
	v_mfma_f32_16x16x128_f8f6f4 v[126:129], v[50:57], v[18:25], v[126:129]
	v_mfma_f32_16x16x128_f8f6f4 v[122:125], v[58:65], v[18:25], v[122:125]
	v_mfma_f32_16x16x128_f8f6f4 v[110:113], v[50:57], v[26:33], v[110:113]
	v_mfma_f32_16x16x128_f8f6f4 v[106:109], v[58:65], v[26:33], v[106:109]
	v_mfma_f32_16x16x128_f8f6f4 v[94:97], v[50:57], v[34:41], v[94:97]
	v_mfma_f32_16x16x128_f8f6f4 v[90:93], v[58:65], v[34:41], v[90:93]
	v_mfma_f32_16x16x128_f8f6f4 v[78:81], v[50:57], v[42:49], v[78:81]
	v_mfma_f32_16x16x128_f8f6f4 v[74:77], v[58:65], v[42:49], v[74:77]
	v_mfma_f32_16x16x128_f8f6f4 v[118:121], v[2:9], v[18:25], v[118:121]
	v_mfma_f32_16x16x128_f8f6f4 v[114:117], v[10:17], v[18:25], v[114:117]
	v_mfma_f32_16x16x128_f8f6f4 v[102:105], v[2:9], v[26:33], v[102:105]
	v_mfma_f32_16x16x128_f8f6f4 v[98:101], v[10:17], v[26:33], v[98:101]
	v_mfma_f32_16x16x128_f8f6f4 v[86:89], v[2:9], v[34:41], v[86:89]
	v_mfma_f32_16x16x128_f8f6f4 v[82:85], v[10:17], v[34:41], v[82:85]
	v_mfma_f32_16x16x128_f8f6f4 v[70:73], v[2:9], v[42:49], v[70:73]
	v_mfma_f32_16x16x128_f8f6f4 v[66:69], v[10:17], v[42:49], v[66:69]
	s_setprio 0
	s_barrier
	s_add_i32 s23, s23, 2
	s_cmp_lt_i32 s23, 12
	s_cbranch_scc1 .Lp9_top
	s_and_b64 vcc, exec, s[40:41]
	s_cbranch_vccz .LBB0_1309
	s_waitcnt vmcnt(8)
	v_lshl_or_b32 v227, v227, 11, v218
	v_lshl_or_b32 v228, v228, 11, v218
	v_lshl_or_b32 v229, v229, 11, v218
	v_lshl_or_b32 v230, v230, 11, v218
	s_branch .LBB0_1309

; __device__ __forceinline__ float sigmoidf_(float x) { return __builtin_amdgcn_rcpf(1.0f + __builtin_amdgcn_exp2f(-1.44269504089f * x)); }
;     __device__ __forceinline__ void operator()(EPI_ARGS) const {
;         const int j0 = u.pn * 128 + wc * 32 + 8 * fq; const float* bb = b1 + (size_t)u.e * 2 * FE;
;         const f32x4 ba0 = *(const f32x4*)(bb + j0), ba1 = *(const f32x4*)(bb + j0 + 4), bl0 = *(const f32x4*)(bb + FE + j0), bl1 = *(const f32x4*)(bb + FE + j0 + 4);
;         const int j0q = u.pn * 128 + wc * 32 + 8 * (fq & ~1);
; #pragma unroll
;         for (int ai = 0; ai < 2; ++ai)
; #pragma unroll
;             for (int mp = 0; mp < 2; ++mp) { unsigned px[2], py[2];
; #pragma unroll
;                 for (int h = 0; h < 2; ++h) { const int m = 2 * mp + h;
;                     const f32x4 a0 = acc[ai][0][m][0] * 0.03125f + ba0, a1 = acc[ai][0][m][1] * 0.03125f + ba1, l0 = acc[ai][1][m][0] * 0.03125f + bl0, l1 = acc[ai][1][m][1] * 0.03125f + bl1;
;                     float o[8];
; #pragma unroll
;                     for (int j = 0; j < 4; ++j) { const float g0 = fminf(a0[j], 7.0f), g1 = fminf(a1[j], 7.0f), x0 = fminf(fmaxf(l0[j], -7.0f), 7.0f), x1 = fminf(fmaxf(l1[j], -7.0f), 7.0f);
;                         o[j] = g0 * sigmoidf_(1.702f * g0) * (x0 + 1.0f); o[4 + j] = g1 * sigmoidf_(1.702f * g1) * (x1 + 1.0f); }
;                     px[h] = pk4_fp8(o[0], o[1], o[2], o[3]); py[h] = pk4_fp8(o[4], o[5], o[6], o[7]); }
;                 const u32x4 q = pair16(px[0], py[0], px[1], py[1]);
;                 const int row = u.pm * 256 + ai * 128 + wr * 64 + (2 * mp + (fq & 1)) * 16 + fr;
;                 *(u32x4*)(ACT + (size_t)row * FE + j0q) = q; }
.LBB0_1334:
	s_lshl_b32 s8, s30, 7
	s_or_b32 s10, s8, s69
	s_lshl_b32 s8, s81, 8
	s_nop 15
	v_mov_b64_e32 v[10:11], v[240:241]
	v_mov_b64_e32 v[12:13], v[242:243]
	v_mov_b64_e32 v[6:7], v[244:245]
	v_mov_b64_e32 v[8:9], v[246:247]
	v_mov_b64_e32 v[14:15], v[248:249]
	v_mov_b64_e32 v[16:17], v[250:251]
	v_mov_b64_e32 v[2:3], v[252:253]
	v_mov_b32_e32 v4, v255
	v_mov_b32_e32 v5, v239
	s_waitcnt lgkmcnt(0)
	v_or_b32_e32 v18, s10, v207
	v_ashrrev_i32_e32 v19, 31, v18
	s_and_b64 vcc, exec, s[6:7]
	s_mov_b64 s[6:7], -1
	v_fmamk_f32 v20, v190, 0x3d000000, v10
	v_min_f32_e32 v20, 0x40e00000, v20
	v_mul_f32_e32 v30, 0x3fd9db23, v20
	v_mul_f32_e32 v30, 0xbfb8aa3b, v30
	v_exp_f32_e32 v30, v30
	v_fmamk_f32 v21, v186, 0x3d000000, v6
	v_min_f32_e32 v21, 0x40e00000, v21
	v_mul_f32_e32 v31, 0x3fd9db23, v21
	v_mul_f32_e32 v31, 0xbfb8aa3b, v31
	v_add_f32_e32 v30, 1.0, v30
	v_exp_f32_e32 v31, v31
	v_rcp_f32_e32 v30, v30
	v_fmamk_f32 v22, v191, 0x3d000000, v11
	v_fmamk_f32 v23, v187, 0x3d000000, v7
	v_fmamk_f32 v27, v189, 0x3d000000, v9
	v_min_f32_e32 v22, 0x40e00000, v22
	v_min_f32_e32 v23, 0x40e00000, v23
	v_min_f32_e32 v27, 0x40e00000, v27
	v_mul_f32_e32 v34, 0x3fd9db23, v22
	v_mul_f32_e32 v35, 0x3fd9db23, v23
	v_mul_f32_e32 v34, 0xbfb8aa3b, v34
	v_add_f32_e32 v31, 1.0, v31
	v_mul_f32_e32 v20, v20, v30
	v_mul_f32_e32 v30, 0x3fd9db23, v27
	v_mul_f32_e32 v35, 0xbfb8aa3b, v35
	v_exp_f32_e32 v34, v34
	v_rcp_f32_e32 v31, v31
	v_mul_f32_e32 v30, 0xbfb8aa3b, v30
	v_fmamk_f32 v25, v188, 0x3d000000, v8
	v_exp_f32_e32 v35, v35
	v_exp_f32_e32 v30, v30
	v_min_f32_e32 v25, 0x40e00000, v25
	v_fmamk_f32 v29, v178, 0x3d000000, v2
	v_fmamk_f32 v24, v192, 0x3d000000, v12
	v_fmamk_f32 v26, v193, 0x3d000000, v13
	v_mul_f32_e32 v39, 0x3fd9db23, v25
	v_med3_f32 v29, v29, s76, v225
	v_min_f32_e32 v24, 0x40e00000, v24
	v_min_f32_e32 v26, 0x40e00000, v26
	v_mul_f32_e32 v39, 0xbfb8aa3b, v39
	v_add_f32_e32 v29, 1.0, v29
	v_add_f32_e32 v34, 1.0, v34
	v_mul_f32_e32 v21, v21, v31
	v_fmamk_f32 v28, v182, 0x3d000000, v14
	v_mul_f32_e32 v38, 0x3fd9db23, v24
	v_exp_f32_e32 v39, v39
	v_add_f32_e32 v35, 1.0, v35
	v_rcp_f32_e32 v34, v34
	v_mul_f32_e32 v21, v29, v21
	v_mul_f32_e32 v29, 0x3fd9db23, v26
	v_add_f32_e32 v30, 1.0, v30
	v_med3_f32 v28, v28, s76, v225
	v_mul_f32_e32 v38, 0xbfb8aa3b, v38
	v_rcp_f32_e32 v35, v35
	v_mul_f32_e32 v29, 0xbfb8aa3b, v29
	v_rcp_f32_e32 v30, v30
	v_fmamk_f32 v32, v183, 0x3d000000, v15
	v_add_f32_e32 v28, 1.0, v28
	v_exp_f32_e32 v38, v38
	v_exp_f32_e32 v29, v29
	v_fmamk_f32 v33, v179, 0x3d000000, v3
	v_med3_f32 v32, v32, s76, v225
	v_mul_f32_e32 v20, v28, v20
	v_fmamk_f32 v28, v181, 0x3d000000, v5
	v_med3_f32 v33, v33, s76, v225
	v_add_f32_e32 v32, 1.0, v32
	v_add_f32_e32 v39, 1.0, v39
	v_mul_f32_e32 v22, v22, v34
	v_med3_f32 v28, v28, s76, v225
	v_add_f32_e32 v33, 1.0, v33
	v_rcp_f32_e32 v39, v39
	v_mul_f32_e32 v23, v23, v35
	v_mul_f32_e32 v22, v32, v22
	v_mul_f32_e32 v27, v27, v30
	v_add_f32_e32 v28, 1.0, v28
	v_add_f32_e32 v38, 1.0, v38
	v_mul_f32_e32 v23, v33, v23
	v_add_f32_e32 v29, 1.0, v29
	v_mul_f32_e32 v27, v28, v27
	v_med3_f32 v20, v20, s77, v226
	v_med3_f32 v28, v22, s77, v226
	v_mov_b32_e32 v22, v201
	v_fmamk_f32 v37, v180, 0x3d000000, v4
	v_rcp_f32_e32 v38, v38
	v_rcp_f32_e32 v29, v29
	v_cvt_pk_fp8_f32 v22, v20, v28
	v_med3_f32 v20, v21, s77, v226
	v_med3_f32 v21, v23, s77, v226
	v_mov_b32_e32 v23, v201
	v_med3_f32 v37, v37, s76, v225
	v_cvt_pk_fp8_f32 v23, v20, v21
	v_fmamk_f32 v36, v184, 0x3d000000, v16
	v_fmamk_f32 v40, v185, 0x3d000000, v17
	v_add_f32_e32 v37, 1.0, v37
	v_mul_f32_e32 v25, v25, v39
	v_med3_f32 v36, v36, s76, v225
	v_med3_f32 v40, v40, s76, v225
	v_mul_f32_e32 v25, v37, v25
	v_add_f32_e32 v36, 1.0, v36
	v_mul_f32_e32 v24, v24, v38
	v_mul_f32_e32 v26, v26, v29
	v_add_f32_e32 v29, 1.0, v40
	v_med3_f32 v20, v25, s77, v226
	v_med3_f32 v21, v27, s77, v226
	v_mul_f32_e32 v24, v36, v24
	v_mul_f32_e32 v26, v29, v26
	v_cvt_pk_fp8_f32 v23, v20, v21 op_sel:[0,0,1]
	v_fmamk_f32 v20, v174, 0x3d000000, v10
	v_med3_f32 v24, v24, s77, v226
	v_med3_f32 v26, v26, s77, v226
	v_min_f32_e32 v20, 0x40e00000, v20
	v_fmamk_f32 v21, v170, 0x3d000000, v6
	v_cvt_pk_fp8_f32 v22, v24, v26 op_sel:[0,0,1]
	v_min_f32_e32 v21, 0x40e00000, v21
	v_mul_f32_e32 v26, 0x3fd9db23, v20
	v_mul_f32_e32 v26, 0xbfb8aa3b, v26
	v_mul_f32_e32 v27, 0x3fd9db23, v21
	v_exp_f32_e32 v26, v26
	v_mul_f32_e32 v27, 0xbfb8aa3b, v27
	v_exp_f32_e32 v27, v27
	v_fmamk_f32 v24, v166, 0x3d000000, v14
	v_add_f32_e32 v26, 1.0, v26
	v_rcp_f32_e32 v26, v26
	v_add_f32_e32 v27, 1.0, v27
	v_rcp_f32_e32 v27, v27
	v_med3_f32 v24, v24, s76, v225
	v_fmamk_f32 v25, v162, 0x3d000000, v2
	v_med3_f32 v25, v25, s76, v225
	v_mul_f32_e32 v20, v20, v26
	v_add_f32_e32 v24, 1.0, v24
	v_mul_f32_e32 v20, v24, v20
	v_mul_f32_e32 v21, v21, v27
	v_add_f32_e32 v24, 1.0, v25
	v_mul_f32_e32 v21, v24, v21
	v_fmamk_f32 v24, v175, 0x3d000000, v11
	v_min_f32_e32 v24, 0x40e00000, v24
	v_fmamk_f32 v25, v171, 0x3d000000, v7
	v_min_f32_e32 v25, 0x40e00000, v25
	v_mul_f32_e32 v28, 0x3fd9db23, v24
	v_mul_f32_e32 v28, 0xbfb8aa3b, v28
	v_mul_f32_e32 v29, 0x3fd9db23, v25
	v_exp_f32_e32 v28, v28
	v_mul_f32_e32 v29, 0xbfb8aa3b, v29
	v_exp_f32_e32 v29, v29
	v_fmamk_f32 v26, v167, 0x3d000000, v15
	v_add_f32_e32 v28, 1.0, v28
	v_rcp_f32_e32 v28, v28
	v_add_f32_e32 v29, 1.0, v29
	v_rcp_f32_e32 v29, v29
	v_med3_f32 v26, v26, s76, v225
	v_fmamk_f32 v27, v163, 0x3d000000, v3
	v_med3_f32 v27, v27, s76, v225
	v_mul_f32_e32 v24, v24, v28
	v_add_f32_e32 v26, 1.0, v26
	v_mul_f32_e32 v24, v26, v24
	v_mul_f32_e32 v25, v25, v29
	v_add_f32_e32 v26, 1.0, v27
	v_mul_f32_e32 v25, v26, v25
	v_fmamk_f32 v26, v176, 0x3d000000, v12
	v_min_f32_e32 v26, 0x40e00000, v26
; __device__ __forceinline__ float sigmoidf_(float x) { return __builtin_amdgcn_rcpf(1.0f + __builtin_amdgcn_exp2f(-1.44269504089f * x)); }
;     __device__ __forceinline__ void operator()(EPI_ARGS) const {
;     ...
; #pragma unroll
;         for (int ai = 0; ai < 2; ++ai)
; #pragma unroll
;             for (int mp = 0; mp < 2; ++mp) { unsigned px[2], py[2];
; #pragma unroll
;                 for (int h = 0; h < 2; ++h) { const int m = 2 * mp + h;
;                     const f32x4 a0 = acc[ai][0][m][0] * 0.03125f + ba0, a1 = acc[ai][0][m][1] * 0.03125f + ba1, l0 = acc[ai][1][m][0] * 0.03125f + bl0, l1 = acc[ai][1][m][1] * 0.03125f + bl1;
;                     float o[8];
; #pragma unroll
;                     for (int j = 0; j < 4; ++j) { const float g0 = fminf(a0[j], 7.0f), g1 = fminf(a1[j], 7.0f), x0 = fminf(fmaxf(l0[j], -7.0f), 7.0f), x1 = fminf(fmaxf(l1[j], -7.0f), 7.0f);
;                         o[j] = g0 * sigmoidf_(1.702f * g0) * (x0 + 1.0f); o[4 + j] = g1 * sigmoidf_(1.702f * g1) * (x1 + 1.0f); }
;                     px[h] = pk4_fp8(o[0], o[1], o[2], o[3]); py[h] = pk4_fp8(o[4], o[5], o[6], o[7]); }
;                 const u32x4 q = pair16(px[0], py[0], px[1], py[1]);
;                 const int row = u.pm * 256 + ai * 128 + wr * 64 + (2 * mp + (fq & 1)) * 16 + fr;
;                 *(u32x4*)(ACT + (size_t)row * FE + j0q) = q; }
	v_fmamk_f32 v27, v172, 0x3d000000, v8
	v_min_f32_e32 v27, 0x40e00000, v27
	v_mul_f32_e32 v30, 0x3fd9db23, v26
	v_mul_f32_e32 v30, 0xbfb8aa3b, v30
	v_mul_f32_e32 v31, 0x3fd9db23, v27
	v_exp_f32_e32 v30, v30
	v_mul_f32_e32 v31, 0xbfb8aa3b, v31
	v_exp_f32_e32 v31, v31
	v_fmamk_f32 v28, v168, 0x3d000000, v16
	v_add_f32_e32 v30, 1.0, v30
	v_rcp_f32_e32 v30, v30
	v_add_f32_e32 v31, 1.0, v31
	v_rcp_f32_e32 v31, v31
	v_med3_f32 v28, v28, s76, v225
	v_fmamk_f32 v29, v164, 0x3d000000, v4
	v_med3_f32 v29, v29, s76, v225
	v_mul_f32_e32 v26, v26, v30
	v_add_f32_e32 v28, 1.0, v28
	v_mul_f32_e32 v26, v28, v26
	v_mul_f32_e32 v27, v27, v31
	v_add_f32_e32 v28, 1.0, v29
	v_mul_f32_e32 v27, v28, v27
	v_fmamk_f32 v28, v177, 0x3d000000, v13
	v_min_f32_e32 v28, 0x40e00000, v28
	v_fmamk_f32 v29, v173, 0x3d000000, v9
	v_min_f32_e32 v29, 0x40e00000, v29
	v_mul_f32_e32 v32, 0x3fd9db23, v28
	v_mul_f32_e32 v32, 0xbfb8aa3b, v32
	v_mul_f32_e32 v33, 0x3fd9db23, v29
	v_exp_f32_e32 v32, v32
	v_mul_f32_e32 v33, 0xbfb8aa3b, v33
	v_exp_f32_e32 v33, v33
	v_fmamk_f32 v30, v169, 0x3d000000, v17
	v_add_f32_e32 v32, 1.0, v32
	v_rcp_f32_e32 v32, v32
	v_add_f32_e32 v33, 1.0, v33
	v_rcp_f32_e32 v33, v33
	v_med3_f32 v30, v30, s76, v225
	v_fmamk_f32 v31, v165, 0x3d000000, v5
	v_med3_f32 v31, v31, s76, v225
	v_mul_f32_e32 v28, v28, v32
	v_add_f32_e32 v30, 1.0, v30
	v_mul_f32_e32 v28, v30, v28
	v_mul_f32_e32 v29, v29, v33
	v_add_f32_e32 v30, 1.0, v31
	v_mul_f32_e32 v29, v30, v29
	v_med3_f32 v20, v20, s77, v226
	v_med3_f32 v30, v24, s77, v226
	v_mov_b32_e32 v24, v201
	v_cvt_pk_fp8_f32 v24, v20, v30
	v_med3_f32 v20, v21, s77, v226
	v_med3_f32 v21, v25, s77, v226
	v_mov_b32_e32 v25, v201
	v_cvt_pk_fp8_f32 v25, v20, v21
	v_med3_f32 v26, v26, s77, v226
	v_med3_f32 v28, v28, s77, v226
	v_med3_f32 v20, v27, s77, v226
	v_med3_f32 v21, v29, s77, v226
	v_cvt_pk_fp8_f32 v24, v26, v28 op_sel:[0,0,1]
	v_cvt_pk_fp8_f32 v25, v20, v21 op_sel:[0,0,1]
	v_add_u32_e32 v20, s8, v219
	v_ashrrev_i32_e32 v21, 31, v20
	v_lshlrev_b64 v[26:27], 11, v[20:21]
	v_lshl_add_u64 v[26:27], s[16:17], 0, v[26:27]
	v_permlane16_swap_b32_e32 v22, v24
	v_permlane16_swap_b32_e32 v23, v25
	v_lshl_add_u64 v[26:27], v[26:27], 0, v[18:19]
	v_fmamk_f32 v21, v158, 0x3d000000, v10
	global_store_dwordx4 v[26:27], v[22:25], off
	v_min_f32_e32 v21, 0x40e00000, v21
	s_nop 0
	v_fmamk_f32 v22, v154, 0x3d000000, v6
	v_min_f32_e32 v22, 0x40e00000, v22
	v_mul_f32_e32 v25, 0x3fd9db23, v21
	v_mul_f32_e32 v25, 0xbfb8aa3b, v25
	v_mul_f32_e32 v26, 0x3fd9db23, v22
	v_exp_f32_e32 v25, v25
	v_mul_f32_e32 v26, 0xbfb8aa3b, v26
	v_exp_f32_e32 v26, v26
	v_fmamk_f32 v23, v150, 0x3d000000, v14
	v_add_f32_e32 v25, 1.0, v25
	v_rcp_f32_e32 v25, v25
	v_add_f32_e32 v26, 1.0, v26
	v_rcp_f32_e32 v26, v26
	v_med3_f32 v23, v23, s76, v225
	v_fmamk_f32 v24, v146, 0x3d000000, v2
	v_med3_f32 v24, v24, s76, v225
	v_mul_f32_e32 v21, v21, v25
	v_add_f32_e32 v23, 1.0, v23
	v_mul_f32_e32 v21, v23, v21
	v_mul_f32_e32 v22, v22, v26
	v_add_f32_e32 v23, 1.0, v24
	v_mul_f32_e32 v23, v23, v22
	v_fmamk_f32 v22, v159, 0x3d000000, v11
	v_min_f32_e32 v22, 0x40e00000, v22
	v_fmamk_f32 v24, v155, 0x3d000000, v7
	v_min_f32_e32 v24, 0x40e00000, v24
	v_mul_f32_e32 v27, 0x3fd9db23, v22
	v_mul_f32_e32 v27, 0xbfb8aa3b, v27
	v_mul_f32_e32 v28, 0x3fd9db23, v24
	v_exp_f32_e32 v27, v27
	v_mul_f32_e32 v28, 0xbfb8aa3b, v28
	v_exp_f32_e32 v28, v28
	v_fmamk_f32 v25, v151, 0x3d000000, v15
	v_add_f32_e32 v27, 1.0, v27
	v_rcp_f32_e32 v27, v27
	v_add_f32_e32 v28, 1.0, v28
	v_rcp_f32_e32 v28, v28
	v_med3_f32 v25, v25, s76, v225
	v_fmamk_f32 v26, v147, 0x3d000000, v3
	v_med3_f32 v26, v26, s76, v225
	v_mul_f32_e32 v22, v22, v27
	v_add_f32_e32 v25, 1.0, v25
	v_mul_f32_e32 v22, v25, v22
	v_mul_f32_e32 v24, v24, v28
	v_add_f32_e32 v25, 1.0, v26
	v_mul_f32_e32 v24, v25, v24
	v_fmamk_f32 v25, v160, 0x3d000000, v12
	v_min_f32_e32 v25, 0x40e00000, v25
	v_fmamk_f32 v26, v156, 0x3d000000, v8
	v_min_f32_e32 v26, 0x40e00000, v26
	v_mul_f32_e32 v29, 0x3fd9db23, v25
	v_mul_f32_e32 v29, 0xbfb8aa3b, v29
	v_mul_f32_e32 v30, 0x3fd9db23, v26
	v_exp_f32_e32 v29, v29
	v_mul_f32_e32 v30, 0xbfb8aa3b, v30
	v_exp_f32_e32 v30, v30
	v_fmamk_f32 v27, v152, 0x3d000000, v16
	v_add_f32_e32 v29, 1.0, v29
	v_rcp_f32_e32 v29, v29
	v_add_f32_e32 v30, 1.0, v30
	v_rcp_f32_e32 v30, v30
	v_med3_f32 v27, v27, s76, v225
	v_fmamk_f32 v28, v148, 0x3d000000, v4
	v_med3_f32 v28, v28, s76, v225
	v_mul_f32_e32 v25, v25, v29
	v_add_f32_e32 v27, 1.0, v27
	v_mul_f32_e32 v25, v27, v25
	v_mul_f32_e32 v26, v26, v30
	v_add_f32_e32 v27, 1.0, v28
	v_mul_f32_e32 v26, v27, v26
	v_fmamk_f32 v27, v161, 0x3d000000, v13
	v_min_f32_e32 v27, 0x40e00000, v27
	v_fmamk_f32 v28, v157, 0x3d000000, v9
	v_min_f32_e32 v28, 0x40e00000, v28
	v_mul_f32_e32 v31, 0x3fd9db23, v27
	v_mul_f32_e32 v31, 0xbfb8aa3b, v31
	v_mul_f32_e32 v32, 0x3fd9db23, v28
	v_exp_f32_e32 v31, v31
	v_mul_f32_e32 v32, 0xbfb8aa3b, v32
	v_exp_f32_e32 v32, v32
	v_fmamk_f32 v29, v153, 0x3d000000, v17
	v_add_f32_e32 v31, 1.0, v31
	v_rcp_f32_e32 v31, v31
	v_add_f32_e32 v32, 1.0, v32
	v_rcp_f32_e32 v32, v32
	v_med3_f32 v29, v29, s76, v225
	v_fmamk_f32 v30, v149, 0x3d000000, v5
	v_med3_f32 v30, v30, s76, v225
	v_mul_f32_e32 v27, v27, v31
	v_add_f32_e32 v29, 1.0, v29
	v_mul_f32_e32 v27, v29, v27
	v_mul_f32_e32 v28, v28, v32
	v_add_f32_e32 v29, 1.0, v30
	v_mul_f32_e32 v28, v29, v28
	v_med3_f32 v21, v21, s77, v226
	v_med3_f32 v29, v22, s77, v226
	v_mov_b32_e32 v22, v201
	v_cvt_pk_fp8_f32 v22, v21, v29
	v_med3_f32 v21, v23, s77, v226
	v_med3_f32 v24, v24, s77, v226
	v_mov_b32_e32 v23, v201
	v_cvt_pk_fp8_f32 v23, v21, v24
	v_med3_f32 v21, v26, s77, v226
	v_med3_f32 v24, v28, s77, v226
	v_med3_f32 v25, v25, s77, v226
; __device__ __forceinline__ float sigmoidf_(float x) { return __builtin_amdgcn_rcpf(1.0f + __builtin_amdgcn_exp2f(-1.44269504089f * x)); }
;     __device__ __forceinline__ void operator()(EPI_ARGS) const {
;     ...
; #pragma unroll
;         for (int ai = 0; ai < 2; ++ai)
; #pragma unroll
;             for (int mp = 0; mp < 2; ++mp) { unsigned px[2], py[2];
; #pragma unroll
;                 for (int h = 0; h < 2; ++h) { const int m = 2 * mp + h;
;                     const f32x4 a0 = acc[ai][0][m][0] * 0.03125f + ba0, a1 = acc[ai][0][m][1] * 0.03125f + ba1, l0 = acc[ai][1][m][0] * 0.03125f + bl0, l1 = acc[ai][1][m][1] * 0.03125f + bl1;
;                     float o[8];
; #pragma unroll
;                     for (int j = 0; j < 4; ++j) { const float g0 = fminf(a0[j], 7.0f), g1 = fminf(a1[j], 7.0f), x0 = fminf(fmaxf(l0[j], -7.0f), 7.0f), x1 = fminf(fmaxf(l1[j], -7.0f), 7.0f);
;                         o[j] = g0 * sigmoidf_(1.702f * g0) * (x0 + 1.0f); o[4 + j] = g1 * sigmoidf_(1.702f * g1) * (x1 + 1.0f); }
;                     px[h] = pk4_fp8(o[0], o[1], o[2], o[3]); py[h] = pk4_fp8(o[4], o[5], o[6], o[7]); }
;                 const u32x4 q = pair16(px[0], py[0], px[1], py[1]);
;                 const int row = u.pm * 256 + ai * 128 + wr * 64 + (2 * mp + (fq & 1)) * 16 + fr;
;                 *(u32x4*)(ACT + (size_t)row * FE + j0q) = q; }
	v_cvt_pk_fp8_f32 v23, v21, v24 op_sel:[0,0,1]
	v_fmamk_f32 v21, v142, 0x3d000000, v10
	v_med3_f32 v27, v27, s77, v226
	v_min_f32_e32 v21, 0x40e00000, v21
	v_fmamk_f32 v24, v138, 0x3d000000, v6
	v_cvt_pk_fp8_f32 v22, v25, v27 op_sel:[0,0,1]
	v_min_f32_e32 v24, 0x40e00000, v24
	v_mul_f32_e32 v27, 0x3fd9db23, v21
	v_mul_f32_e32 v27, 0xbfb8aa3b, v27
	v_mul_f32_e32 v28, 0x3fd9db23, v24
	v_exp_f32_e32 v27, v27
	v_mul_f32_e32 v28, 0xbfb8aa3b, v28
	v_exp_f32_e32 v28, v28
	v_fmamk_f32 v25, v134, 0x3d000000, v14
	v_add_f32_e32 v27, 1.0, v27
	v_rcp_f32_e32 v27, v27
	v_add_f32_e32 v28, 1.0, v28
	v_rcp_f32_e32 v28, v28
	v_med3_f32 v25, v25, s76, v225
	v_fmamk_f32 v26, v130, 0x3d000000, v2
	v_med3_f32 v26, v26, s76, v225
	v_mul_f32_e32 v21, v21, v27
	v_add_f32_e32 v25, 1.0, v25
	v_mul_f32_e32 v21, v25, v21
	v_mul_f32_e32 v24, v24, v28
	v_add_f32_e32 v25, 1.0, v26
	v_mul_f32_e32 v25, v25, v24
	v_fmamk_f32 v24, v143, 0x3d000000, v11
	v_min_f32_e32 v24, 0x40e00000, v24
	v_fmamk_f32 v26, v139, 0x3d000000, v7
	v_min_f32_e32 v26, 0x40e00000, v26
	v_mul_f32_e32 v29, 0x3fd9db23, v24
	v_mul_f32_e32 v29, 0xbfb8aa3b, v29
	v_mul_f32_e32 v30, 0x3fd9db23, v26
	v_exp_f32_e32 v29, v29
	v_mul_f32_e32 v30, 0xbfb8aa3b, v30
	v_exp_f32_e32 v30, v30
	v_fmamk_f32 v27, v135, 0x3d000000, v15
	v_add_f32_e32 v29, 1.0, v29
	v_rcp_f32_e32 v29, v29
	v_add_f32_e32 v30, 1.0, v30
	v_rcp_f32_e32 v30, v30
	v_med3_f32 v27, v27, s76, v225
	v_fmamk_f32 v28, v131, 0x3d000000, v3
	v_med3_f32 v28, v28, s76, v225
	v_mul_f32_e32 v24, v24, v29
	v_add_f32_e32 v27, 1.0, v27
	v_mul_f32_e32 v24, v27, v24
	v_mul_f32_e32 v26, v26, v30
	v_add_f32_e32 v27, 1.0, v28
	v_mul_f32_e32 v26, v27, v26
	v_fmamk_f32 v27, v144, 0x3d000000, v12
	v_min_f32_e32 v27, 0x40e00000, v27
	v_fmamk_f32 v28, v140, 0x3d000000, v8
	v_min_f32_e32 v28, 0x40e00000, v28
	v_mul_f32_e32 v31, 0x3fd9db23, v27
	v_mul_f32_e32 v31, 0xbfb8aa3b, v31
	v_mul_f32_e32 v32, 0x3fd9db23, v28
	v_exp_f32_e32 v31, v31
	v_mul_f32_e32 v32, 0xbfb8aa3b, v32
	v_exp_f32_e32 v32, v32
	v_fmamk_f32 v29, v136, 0x3d000000, v16
	v_add_f32_e32 v31, 1.0, v31
	v_rcp_f32_e32 v31, v31
	v_add_f32_e32 v32, 1.0, v32
	v_rcp_f32_e32 v32, v32
	v_med3_f32 v29, v29, s76, v225
	v_fmamk_f32 v30, v132, 0x3d000000, v4
	v_med3_f32 v30, v30, s76, v225
	v_mul_f32_e32 v27, v27, v31
	v_add_f32_e32 v29, 1.0, v29
	v_mul_f32_e32 v27, v29, v27
	v_mul_f32_e32 v28, v28, v32
	v_add_f32_e32 v29, 1.0, v30
	v_mul_f32_e32 v28, v29, v28
	v_fmamk_f32 v29, v145, 0x3d000000, v13
	v_min_f32_e32 v29, 0x40e00000, v29
	v_fmamk_f32 v30, v141, 0x3d000000, v9
	v_min_f32_e32 v30, 0x40e00000, v30
	v_mul_f32_e32 v33, 0x3fd9db23, v29
	v_mul_f32_e32 v33, 0xbfb8aa3b, v33
	v_mul_f32_e32 v34, 0x3fd9db23, v30
	v_exp_f32_e32 v33, v33
	v_mul_f32_e32 v34, 0xbfb8aa3b, v34
	v_exp_f32_e32 v34, v34
	v_fmamk_f32 v31, v137, 0x3d000000, v17
	v_add_f32_e32 v33, 1.0, v33
	v_rcp_f32_e32 v33, v33
	v_add_f32_e32 v34, 1.0, v34
	v_rcp_f32_e32 v34, v34
	v_med3_f32 v31, v31, s76, v225
	v_fmamk_f32 v32, v133, 0x3d000000, v5
	v_med3_f32 v32, v32, s76, v225
	v_mul_f32_e32 v29, v29, v33
	v_add_f32_e32 v31, 1.0, v31
	v_mul_f32_e32 v29, v31, v29
	v_mul_f32_e32 v30, v30, v34
	v_add_f32_e32 v31, 1.0, v32
	v_mul_f32_e32 v30, v31, v30
	v_med3_f32 v21, v21, s77, v226
	v_med3_f32 v31, v24, s77, v226
	v_mov_b32_e32 v24, v201
	v_cvt_pk_fp8_f32 v24, v21, v31
	v_med3_f32 v21, v25, s77, v226
	v_med3_f32 v26, v26, s77, v226
	v_mov_b32_e32 v25, v201
	v_cvt_pk_fp8_f32 v25, v21, v26
	v_med3_f32 v27, v27, s77, v226
	v_med3_f32 v29, v29, s77, v226
	v_med3_f32 v21, v28, s77, v226
	v_med3_f32 v26, v30, s77, v226
	v_cvt_pk_fp8_f32 v24, v27, v29 op_sel:[0,0,1]
	v_cvt_pk_fp8_f32 v25, v21, v26 op_sel:[0,0,1]
	v_add_u32_e32 v26, s8, v220
	v_ashrrev_i32_e32 v27, 31, v26
	v_lshlrev_b64 v[26:27], 11, v[26:27]
	v_lshl_add_u64 v[26:27], s[16:17], 0, v[26:27]
	v_permlane16_swap_b32_e32 v22, v24
	v_permlane16_swap_b32_e32 v23, v25
	v_lshl_add_u64 v[26:27], v[26:27], 0, v[18:19]
	v_fmamk_f32 v21, v126, 0x3d000000, v10
	global_store_dwordx4 v[26:27], v[22:25], off
	v_min_f32_e32 v21, 0x40e00000, v21
	s_nop 0
	v_fmamk_f32 v22, v122, 0x3d000000, v6
	v_min_f32_e32 v22, 0x40e00000, v22
	v_mul_f32_e32 v25, 0x3fd9db23, v21
	v_mul_f32_e32 v25, 0xbfb8aa3b, v25
	v_mul_f32_e32 v26, 0x3fd9db23, v22
	v_exp_f32_e32 v25, v25
	v_mul_f32_e32 v26, 0xbfb8aa3b, v26
	v_exp_f32_e32 v26, v26
	v_fmamk_f32 v23, v118, 0x3d000000, v14
	v_add_f32_e32 v25, 1.0, v25
	v_rcp_f32_e32 v25, v25
	v_add_f32_e32 v26, 1.0, v26
	v_rcp_f32_e32 v26, v26
	v_med3_f32 v23, v23, s76, v225
	v_fmamk_f32 v24, v114, 0x3d000000, v2
	v_med3_f32 v24, v24, s76, v225
	v_mul_f32_e32 v21, v21, v25
	v_add_f32_e32 v23, 1.0, v23
	v_mul_f32_e32 v21, v23, v21
	v_mul_f32_e32 v22, v22, v26
	v_add_f32_e32 v23, 1.0, v24
	v_mul_f32_e32 v23, v23, v22
	v_fmamk_f32 v22, v127, 0x3d000000, v11
	v_min_f32_e32 v22, 0x40e00000, v22
	v_fmamk_f32 v24, v123, 0x3d000000, v7
	v_min_f32_e32 v24, 0x40e00000, v24
	v_mul_f32_e32 v27, 0x3fd9db23, v22
	v_mul_f32_e32 v27, 0xbfb8aa3b, v27
	v_mul_f32_e32 v28, 0x3fd9db23, v24
	v_exp_f32_e32 v27, v27
	v_mul_f32_e32 v28, 0xbfb8aa3b, v28
	v_exp_f32_e32 v28, v28
	v_fmamk_f32 v25, v119, 0x3d000000, v15
	v_add_f32_e32 v27, 1.0, v27
	v_rcp_f32_e32 v27, v27
	v_add_f32_e32 v28, 1.0, v28
	v_rcp_f32_e32 v28, v28
	v_med3_f32 v25, v25, s76, v225
	v_fmamk_f32 v26, v115, 0x3d000000, v3
	v_med3_f32 v26, v26, s76, v225
	v_mul_f32_e32 v22, v22, v27
	v_add_f32_e32 v25, 1.0, v25
	v_mul_f32_e32 v22, v25, v22
	v_mul_f32_e32 v24, v24, v28
	v_add_f32_e32 v25, 1.0, v26
	v_mul_f32_e32 v24, v25, v24
	v_fmamk_f32 v25, v128, 0x3d000000, v12
	v_min_f32_e32 v25, 0x40e00000, v25
	v_fmamk_f32 v26, v124, 0x3d000000, v8
; __device__ __forceinline__ float sigmoidf_(float x) { return __builtin_amdgcn_rcpf(1.0f + __builtin_amdgcn_exp2f(-1.44269504089f * x)); }
;     __device__ __forceinline__ void operator()(EPI_ARGS) const {
;     ...
; #pragma unroll
;         for (int ai = 0; ai < 2; ++ai)
; #pragma unroll
;             for (int mp = 0; mp < 2; ++mp) { unsigned px[2], py[2];
; #pragma unroll
;                 for (int h = 0; h < 2; ++h) { const int m = 2 * mp + h;
;                     const f32x4 a0 = acc[ai][0][m][0] * 0.03125f + ba0, a1 = acc[ai][0][m][1] * 0.03125f + ba1, l0 = acc[ai][1][m][0] * 0.03125f + bl0, l1 = acc[ai][1][m][1] * 0.03125f + bl1;
;                     float o[8];
; #pragma unroll
;                     for (int j = 0; j < 4; ++j) { const float g0 = fminf(a0[j], 7.0f), g1 = fminf(a1[j], 7.0f), x0 = fminf(fmaxf(l0[j], -7.0f), 7.0f), x1 = fminf(fmaxf(l1[j], -7.0f), 7.0f);
;                         o[j] = g0 * sigmoidf_(1.702f * g0) * (x0 + 1.0f); o[4 + j] = g1 * sigmoidf_(1.702f * g1) * (x1 + 1.0f); }
;                     px[h] = pk4_fp8(o[0], o[1], o[2], o[3]); py[h] = pk4_fp8(o[4], o[5], o[6], o[7]); }
;                 const u32x4 q = pair16(px[0], py[0], px[1], py[1]);
;                 const int row = u.pm * 256 + ai * 128 + wr * 64 + (2 * mp + (fq & 1)) * 16 + fr;
;                 *(u32x4*)(ACT + (size_t)row * FE + j0q) = q; }
	v_min_f32_e32 v26, 0x40e00000, v26
	v_mul_f32_e32 v29, 0x3fd9db23, v25
	v_mul_f32_e32 v29, 0xbfb8aa3b, v29
	v_mul_f32_e32 v30, 0x3fd9db23, v26
	v_exp_f32_e32 v29, v29
	v_mul_f32_e32 v30, 0xbfb8aa3b, v30
	v_exp_f32_e32 v30, v30
	v_fmamk_f32 v27, v120, 0x3d000000, v16
	v_add_f32_e32 v29, 1.0, v29
	v_rcp_f32_e32 v29, v29
	v_add_f32_e32 v30, 1.0, v30
	v_rcp_f32_e32 v30, v30
	v_med3_f32 v27, v27, s76, v225
	v_fmamk_f32 v28, v116, 0x3d000000, v4
	v_med3_f32 v28, v28, s76, v225
	v_mul_f32_e32 v25, v25, v29
	v_add_f32_e32 v27, 1.0, v27
	v_mul_f32_e32 v25, v27, v25
	v_mul_f32_e32 v26, v26, v30
	v_add_f32_e32 v27, 1.0, v28
	v_mul_f32_e32 v26, v27, v26
	v_fmamk_f32 v27, v129, 0x3d000000, v13
	v_min_f32_e32 v27, 0x40e00000, v27
	v_fmamk_f32 v28, v125, 0x3d000000, v9
	v_min_f32_e32 v28, 0x40e00000, v28
	v_mul_f32_e32 v31, 0x3fd9db23, v27
	v_mul_f32_e32 v31, 0xbfb8aa3b, v31
	v_mul_f32_e32 v32, 0x3fd9db23, v28
	v_exp_f32_e32 v31, v31
	v_mul_f32_e32 v32, 0xbfb8aa3b, v32
	v_exp_f32_e32 v32, v32
	v_fmamk_f32 v29, v121, 0x3d000000, v17
	v_add_f32_e32 v31, 1.0, v31
	v_rcp_f32_e32 v31, v31
	v_add_f32_e32 v32, 1.0, v32
	v_rcp_f32_e32 v32, v32
	v_med3_f32 v29, v29, s76, v225
	v_fmamk_f32 v30, v117, 0x3d000000, v5
	v_med3_f32 v30, v30, s76, v225
	v_mul_f32_e32 v27, v27, v31
	v_add_f32_e32 v29, 1.0, v29
	v_mul_f32_e32 v27, v29, v27
	v_mul_f32_e32 v28, v28, v32
	v_add_f32_e32 v29, 1.0, v30
	v_mul_f32_e32 v28, v29, v28
	v_med3_f32 v21, v21, s77, v226
	v_med3_f32 v29, v22, s77, v226
	v_mov_b32_e32 v22, v201
	v_cvt_pk_fp8_f32 v22, v21, v29
	v_med3_f32 v21, v23, s77, v226
	v_med3_f32 v24, v24, s77, v226
	v_mov_b32_e32 v23, v201
	v_cvt_pk_fp8_f32 v23, v21, v24
	v_med3_f32 v21, v26, s77, v226
	v_med3_f32 v24, v28, s77, v226
	v_med3_f32 v25, v25, s77, v226
	v_cvt_pk_fp8_f32 v23, v21, v24 op_sel:[0,0,1]
	v_fmamk_f32 v21, v110, 0x3d000000, v10
	v_med3_f32 v27, v27, s77, v226
	v_min_f32_e32 v21, 0x40e00000, v21
	v_fmamk_f32 v24, v106, 0x3d000000, v6
	v_cvt_pk_fp8_f32 v22, v25, v27 op_sel:[0,0,1]
	v_min_f32_e32 v24, 0x40e00000, v24
	v_mul_f32_e32 v27, 0x3fd9db23, v21
	v_mul_f32_e32 v27, 0xbfb8aa3b, v27
	v_mul_f32_e32 v28, 0x3fd9db23, v24
	v_exp_f32_e32 v27, v27
	v_mul_f32_e32 v28, 0xbfb8aa3b, v28
	v_exp_f32_e32 v28, v28
	v_fmamk_f32 v25, v102, 0x3d000000, v14
	v_add_f32_e32 v27, 1.0, v27
	v_rcp_f32_e32 v27, v27
	v_add_f32_e32 v28, 1.0, v28
	v_rcp_f32_e32 v28, v28
	v_med3_f32 v25, v25, s76, v225
	v_fmamk_f32 v26, v98, 0x3d000000, v2
	v_med3_f32 v26, v26, s76, v225
	v_mul_f32_e32 v21, v21, v27
	v_add_f32_e32 v25, 1.0, v25
	v_mul_f32_e32 v21, v25, v21
	v_mul_f32_e32 v24, v24, v28
	v_add_f32_e32 v25, 1.0, v26
	v_mul_f32_e32 v25, v25, v24
	v_fmamk_f32 v24, v111, 0x3d000000, v11
	v_min_f32_e32 v24, 0x40e00000, v24
	v_fmamk_f32 v26, v107, 0x3d000000, v7
	v_min_f32_e32 v26, 0x40e00000, v26
	v_mul_f32_e32 v29, 0x3fd9db23, v24
	v_mul_f32_e32 v29, 0xbfb8aa3b, v29
	v_mul_f32_e32 v30, 0x3fd9db23, v26
	v_exp_f32_e32 v29, v29
	v_mul_f32_e32 v30, 0xbfb8aa3b, v30
	v_exp_f32_e32 v30, v30
	v_fmamk_f32 v27, v103, 0x3d000000, v15
	v_add_f32_e32 v29, 1.0, v29
	v_rcp_f32_e32 v29, v29
	v_add_f32_e32 v30, 1.0, v30
	v_rcp_f32_e32 v30, v30
	v_med3_f32 v27, v27, s76, v225
	v_fmamk_f32 v28, v99, 0x3d000000, v3
	v_med3_f32 v28, v28, s76, v225
	v_mul_f32_e32 v24, v24, v29
	v_add_f32_e32 v27, 1.0, v27
	v_mul_f32_e32 v24, v27, v24
	v_mul_f32_e32 v26, v26, v30
	v_add_f32_e32 v27, 1.0, v28
	v_mul_f32_e32 v26, v27, v26
	v_fmamk_f32 v27, v112, 0x3d000000, v12
	v_min_f32_e32 v27, 0x40e00000, v27
	v_fmamk_f32 v28, v108, 0x3d000000, v8
	v_min_f32_e32 v28, 0x40e00000, v28
	v_mul_f32_e32 v31, 0x3fd9db23, v27
	v_mul_f32_e32 v31, 0xbfb8aa3b, v31
	v_mul_f32_e32 v32, 0x3fd9db23, v28
	v_exp_f32_e32 v31, v31
	v_mul_f32_e32 v32, 0xbfb8aa3b, v32
	v_exp_f32_e32 v32, v32
	v_fmamk_f32 v29, v104, 0x3d000000, v16
	v_add_f32_e32 v31, 1.0, v31
	v_rcp_f32_e32 v31, v31
	v_add_f32_e32 v32, 1.0, v32
	v_rcp_f32_e32 v32, v32
	v_med3_f32 v29, v29, s76, v225
	v_fmamk_f32 v30, v100, 0x3d000000, v4
	v_med3_f32 v30, v30, s76, v225
	v_mul_f32_e32 v27, v27, v31
	v_add_f32_e32 v29, 1.0, v29
	v_mul_f32_e32 v27, v29, v27
	v_mul_f32_e32 v28, v28, v32
	v_add_f32_e32 v29, 1.0, v30
	v_mul_f32_e32 v28, v29, v28
	v_fmamk_f32 v29, v113, 0x3d000000, v13
	v_min_f32_e32 v29, 0x40e00000, v29
	v_fmamk_f32 v30, v109, 0x3d000000, v9
	v_min_f32_e32 v30, 0x40e00000, v30
	v_mul_f32_e32 v33, 0x3fd9db23, v29
	v_mul_f32_e32 v33, 0xbfb8aa3b, v33
	v_mul_f32_e32 v34, 0x3fd9db23, v30
	v_exp_f32_e32 v33, v33
	v_mul_f32_e32 v34, 0xbfb8aa3b, v34
	v_exp_f32_e32 v34, v34
	v_fmamk_f32 v31, v105, 0x3d000000, v17
	v_add_f32_e32 v33, 1.0, v33
	v_rcp_f32_e32 v33, v33
	v_add_f32_e32 v34, 1.0, v34
	v_rcp_f32_e32 v34, v34
	v_med3_f32 v31, v31, s76, v225
	v_fmamk_f32 v32, v101, 0x3d000000, v5
	v_med3_f32 v32, v32, s76, v225
	v_mul_f32_e32 v29, v29, v33
	v_add_f32_e32 v31, 1.0, v31
	v_mul_f32_e32 v29, v31, v29
	v_mul_f32_e32 v30, v30, v34
	v_add_f32_e32 v31, 1.0, v32
	v_mul_f32_e32 v30, v31, v30
	v_med3_f32 v21, v21, s77, v226
	v_med3_f32 v31, v24, s77, v226
	v_mov_b32_e32 v24, v201
	v_cvt_pk_fp8_f32 v24, v21, v31
	v_med3_f32 v21, v25, s77, v226
	v_med3_f32 v26, v26, s77, v226
	v_mov_b32_e32 v25, v201
	v_cvt_pk_fp8_f32 v25, v21, v26
	v_med3_f32 v27, v27, s77, v226
	v_med3_f32 v29, v29, s77, v226
	v_med3_f32 v21, v28, s77, v226
	v_med3_f32 v26, v30, s77, v226
	v_cvt_pk_fp8_f32 v24, v27, v29 op_sel:[0,0,1]
	v_cvt_pk_fp8_f32 v25, v21, v26 op_sel:[0,0,1]
	v_add_u32_e32 v26, 0x80, v20
	v_ashrrev_i32_e32 v27, 31, v26
	v_lshlrev_b64 v[26:27], 11, v[26:27]
	v_lshl_add_u64 v[26:27], s[16:17], 0, v[26:27]
	v_permlane16_swap_b32_e32 v22, v24
	v_permlane16_swap_b32_e32 v23, v25
; __device__ __forceinline__ float sigmoidf_(float x) { return __builtin_amdgcn_rcpf(1.0f + __builtin_amdgcn_exp2f(-1.44269504089f * x)); }
;     __device__ __forceinline__ void operator()(EPI_ARGS) const {
;     ...
; #pragma unroll
;         for (int ai = 0; ai < 2; ++ai)
; #pragma unroll
;             for (int mp = 0; mp < 2; ++mp) { unsigned px[2], py[2];
; #pragma unroll
;                 for (int h = 0; h < 2; ++h) { const int m = 2 * mp + h;
;                     const f32x4 a0 = acc[ai][0][m][0] * 0.03125f + ba0, a1 = acc[ai][0][m][1] * 0.03125f + ba1, l0 = acc[ai][1][m][0] * 0.03125f + bl0, l1 = acc[ai][1][m][1] * 0.03125f + bl1;
;                     float o[8];
; #pragma unroll
;                     for (int j = 0; j < 4; ++j) { const float g0 = fminf(a0[j], 7.0f), g1 = fminf(a1[j], 7.0f), x0 = fminf(fmaxf(l0[j], -7.0f), 7.0f), x1 = fminf(fmaxf(l1[j], -7.0f), 7.0f);
;                         o[j] = g0 * sigmoidf_(1.702f * g0) * (x0 + 1.0f); o[4 + j] = g1 * sigmoidf_(1.702f * g1) * (x1 + 1.0f); }
;                     px[h] = pk4_fp8(o[0], o[1], o[2], o[3]); py[h] = pk4_fp8(o[4], o[5], o[6], o[7]); }
;                 const u32x4 q = pair16(px[0], py[0], px[1], py[1]);
;                 const int row = u.pm * 256 + ai * 128 + wr * 64 + (2 * mp + (fq & 1)) * 16 + fr;
;                 *(u32x4*)(ACT + (size_t)row * FE + j0q) = q; }
	v_lshl_add_u64 v[26:27], v[26:27], 0, v[18:19]
	v_fmamk_f32 v21, v94, 0x3d000000, v10
	global_store_dwordx4 v[26:27], v[22:25], off
	v_min_f32_e32 v21, 0x40e00000, v21
	v_fmamk_f32 v10, v78, 0x3d000000, v10
	v_fmamk_f32 v22, v90, 0x3d000000, v6
	v_min_f32_e32 v22, 0x40e00000, v22
	v_mul_f32_e32 v25, 0x3fd9db23, v21
	v_mul_f32_e32 v25, 0xbfb8aa3b, v25
	v_mul_f32_e32 v26, 0x3fd9db23, v22
	v_exp_f32_e32 v25, v25
	v_mul_f32_e32 v26, 0xbfb8aa3b, v26
	v_exp_f32_e32 v26, v26
	v_fmamk_f32 v23, v86, 0x3d000000, v14
	v_add_f32_e32 v25, 1.0, v25
	v_rcp_f32_e32 v25, v25
	v_add_f32_e32 v26, 1.0, v26
	v_rcp_f32_e32 v26, v26
	v_med3_f32 v23, v23, s76, v225
	v_fmamk_f32 v24, v82, 0x3d000000, v2
	v_med3_f32 v24, v24, s76, v225
	v_mul_f32_e32 v21, v21, v25
	v_add_f32_e32 v23, 1.0, v23
	v_mul_f32_e32 v21, v23, v21
	v_mul_f32_e32 v22, v22, v26
	v_add_f32_e32 v23, 1.0, v24
	v_mul_f32_e32 v23, v23, v22
	v_fmamk_f32 v22, v95, 0x3d000000, v11
	v_min_f32_e32 v22, 0x40e00000, v22
	v_fmamk_f32 v24, v91, 0x3d000000, v7
	v_min_f32_e32 v24, 0x40e00000, v24
	v_mul_f32_e32 v27, 0x3fd9db23, v22
	v_mul_f32_e32 v27, 0xbfb8aa3b, v27
	v_mul_f32_e32 v28, 0x3fd9db23, v24
	v_exp_f32_e32 v27, v27
	v_mul_f32_e32 v28, 0xbfb8aa3b, v28
	v_exp_f32_e32 v28, v28
	v_fmamk_f32 v25, v87, 0x3d000000, v15
	v_add_f32_e32 v27, 1.0, v27
	v_rcp_f32_e32 v27, v27
	v_add_f32_e32 v28, 1.0, v28
	v_rcp_f32_e32 v28, v28
	v_med3_f32 v25, v25, s76, v225
	v_fmamk_f32 v26, v83, 0x3d000000, v3
	v_med3_f32 v26, v26, s76, v225
	v_mul_f32_e32 v22, v22, v27
	v_add_f32_e32 v25, 1.0, v25
	v_mul_f32_e32 v22, v25, v22
	v_mul_f32_e32 v24, v24, v28
	v_add_f32_e32 v25, 1.0, v26
	v_mul_f32_e32 v24, v25, v24
	v_fmamk_f32 v25, v96, 0x3d000000, v12
	v_min_f32_e32 v25, 0x40e00000, v25
	v_fmamk_f32 v26, v92, 0x3d000000, v8
	v_min_f32_e32 v26, 0x40e00000, v26
	v_mul_f32_e32 v29, 0x3fd9db23, v25
	v_mul_f32_e32 v29, 0xbfb8aa3b, v29
	v_mul_f32_e32 v30, 0x3fd9db23, v26
	v_exp_f32_e32 v29, v29
	v_mul_f32_e32 v30, 0xbfb8aa3b, v30
	v_exp_f32_e32 v30, v30
	v_fmamk_f32 v27, v88, 0x3d000000, v16
	v_add_f32_e32 v29, 1.0, v29
	v_rcp_f32_e32 v29, v29
	v_add_f32_e32 v30, 1.0, v30
	v_rcp_f32_e32 v30, v30
	v_med3_f32 v27, v27, s76, v225
	v_fmamk_f32 v28, v84, 0x3d000000, v4
	v_med3_f32 v28, v28, s76, v225
	v_mul_f32_e32 v25, v25, v29
	v_add_f32_e32 v27, 1.0, v27
	v_mul_f32_e32 v25, v27, v25
	v_mul_f32_e32 v26, v26, v30
	v_add_f32_e32 v27, 1.0, v28
	v_mul_f32_e32 v26, v27, v26
	v_fmamk_f32 v27, v97, 0x3d000000, v13
	v_min_f32_e32 v27, 0x40e00000, v27
	v_fmamk_f32 v28, v93, 0x3d000000, v9
	v_min_f32_e32 v28, 0x40e00000, v28
	v_mul_f32_e32 v31, 0x3fd9db23, v27
	v_mul_f32_e32 v31, 0xbfb8aa3b, v31
	v_mul_f32_e32 v32, 0x3fd9db23, v28
	v_exp_f32_e32 v31, v31
	v_mul_f32_e32 v32, 0xbfb8aa3b, v32
	v_exp_f32_e32 v32, v32
	v_fmamk_f32 v29, v89, 0x3d000000, v17
	v_add_f32_e32 v31, 1.0, v31
	v_rcp_f32_e32 v31, v31
	v_add_f32_e32 v32, 1.0, v32
	v_rcp_f32_e32 v32, v32
	v_med3_f32 v29, v29, s76, v225
	v_fmamk_f32 v30, v85, 0x3d000000, v5
	v_med3_f32 v30, v30, s76, v225
	v_mul_f32_e32 v27, v27, v31
	v_add_f32_e32 v29, 1.0, v29
	v_mul_f32_e32 v27, v29, v27
	v_mul_f32_e32 v28, v28, v32
	v_add_f32_e32 v29, 1.0, v30
	v_mul_f32_e32 v28, v29, v28
	v_med3_f32 v21, v21, s77, v226
	v_med3_f32 v29, v22, s77, v226
	v_mov_b32_e32 v22, v201
	v_cvt_pk_fp8_f32 v22, v21, v29
	v_med3_f32 v21, v23, s77, v226
	v_med3_f32 v24, v24, s77, v226
	v_mov_b32_e32 v23, v201
	v_cvt_pk_fp8_f32 v23, v21, v24
	v_fmamk_f32 v6, v74, 0x3d000000, v6
	v_med3_f32 v21, v26, s77, v226
	v_med3_f32 v24, v28, s77, v226
	v_min_f32_e32 v6, 0x40e00000, v6
	v_cvt_pk_fp8_f32 v23, v21, v24 op_sel:[0,0,1]
	v_mul_f32_e32 v24, 0x3fd9db23, v6
	v_min_f32_e32 v10, 0x40e00000, v10
; __device__ __forceinline__ float sigmoidf_(float x) { return __builtin_amdgcn_rcpf(1.0f + __builtin_amdgcn_exp2f(-1.44269504089f * x)); }
; #define PG8_BAR __builtin_amdgcn_s_barrier()
;     ...
;         if (!has_next) break;
; #pragma unroll
;         for (int a = 0; a < 2; ++a)
; #pragma unroll
;             for (int b = 0; b < 2; ++b)
; #pragma unroll
;                 for (int m = 0; m < 4; ++m)
; #pragma unroll
;                     for (int n = 0; n < 2; ++n) acc[a][b][m][n] = (f32x4){0.f, 0.f, 0.f, 0.f};
;         cur = nxt; cA = nA; cB = nB; rotc = rotn; ++ui;
; #pragma unroll
;         for (int h = 0; h < 2; ++h)
; #pragma unroll
;             for (int i = 0; i < 2; ++i) gcur[h][i] = gnxt[h][i];
;         if (wr == 1) PG8_BAR;
;     }
;     __device__ __forceinline__ void operator()(EPI_ARGS) const {
;     ...
;                 for (int h = 0; h < 2; ++h) { const int m = 2 * mp + h;
;                     const f32x4 a0 = acc[ai][0][m][0] * 0.03125f + ba0, a1 = acc[ai][0][m][1] * 0.03125f + ba1, l0 = acc[ai][1][m][0] * 0.03125f + bl0, l1 = acc[ai][1][m][1] * 0.03125f + bl1;
;                     float o[8];
; #pragma unroll
;                     for (int j = 0; j < 4; ++j) { const float g0 = fminf(a0[j], 7.0f), g1 = fminf(a1[j], 7.0f), x0 = fminf(fmaxf(l0[j], -7.0f), 7.0f), x1 = fminf(fmaxf(l1[j], -7.0f), 7.0f);
;                         o[j] = g0 * sigmoidf_(1.702f * g0) * (x0 + 1.0f); o[4 + j] = g1 * sigmoidf_(1.702f * g1) * (x1 + 1.0f); }
;                     px[h] = pk4_fp8(o[0], o[1], o[2], o[3]); py[h] = pk4_fp8(o[4], o[5], o[6], o[7]); }
;                 const u32x4 q = pair16(px[0], py[0], px[1], py[1]);
;                 const int row = u.pm * 256 + ai * 128 + wr * 64 + (2 * mp + (fq & 1)) * 16 + fr;
;                 *(u32x4*)(ACT + (size_t)row * FE + j0q) = q; }
	v_mul_f32_e32 v24, 0xbfb8aa3b, v24
	v_mul_f32_e32 v21, 0x3fd9db23, v10
	v_exp_f32_e32 v24, v24
	v_mul_f32_e32 v21, 0xbfb8aa3b, v21
	v_exp_f32_e32 v21, v21
	v_fmamk_f32 v2, v66, 0x3d000000, v2
	v_add_f32_e32 v24, 1.0, v24
	v_rcp_f32_e32 v24, v24
	v_add_f32_e32 v21, 1.0, v21
	v_rcp_f32_e32 v21, v21
	v_med3_f32 v2, v2, s76, v225
	v_fmamk_f32 v14, v70, 0x3d000000, v14
	v_mul_f32_e32 v6, v6, v24
	v_add_f32_e32 v2, 1.0, v2
	v_med3_f32 v14, v14, s76, v225
	v_mul_f32_e32 v2, v2, v6
	v_fmamk_f32 v6, v79, 0x3d000000, v11
	v_mul_f32_e32 v10, v10, v21
	v_add_f32_e32 v14, 1.0, v14
	v_min_f32_e32 v6, 0x40e00000, v6
	v_fmamk_f32 v7, v75, 0x3d000000, v7
	v_mul_f32_e32 v10, v14, v10
	v_min_f32_e32 v7, 0x40e00000, v7
	v_mul_f32_e32 v14, 0x3fd9db23, v6
	v_fmamk_f32 v11, v71, 0x3d000000, v15
	v_mul_f32_e32 v14, 0xbfb8aa3b, v14
	v_mul_f32_e32 v15, 0x3fd9db23, v7
	v_exp_f32_e32 v14, v14
	v_mul_f32_e32 v15, 0xbfb8aa3b, v15
	v_exp_f32_e32 v15, v15
	v_fmamk_f32 v8, v76, 0x3d000000, v8
	v_add_f32_e32 v14, 1.0, v14
	v_rcp_f32_e32 v14, v14
	v_add_f32_e32 v15, 1.0, v15
	v_rcp_f32_e32 v15, v15
	v_fmamk_f32 v3, v67, 0x3d000000, v3
	v_min_f32_e32 v8, 0x40e00000, v8
	v_med3_f32 v3, v3, s76, v225
	v_mul_f32_e32 v6, v6, v14
	v_mul_f32_e32 v14, 0x3fd9db23, v8
	v_mul_f32_e32 v7, v7, v15
	v_add_f32_e32 v3, 1.0, v3
	v_mul_f32_e32 v14, 0xbfb8aa3b, v14
	v_mul_f32_e32 v3, v3, v7
	v_fmamk_f32 v7, v80, 0x3d000000, v12
	v_exp_f32_e32 v14, v14
	v_min_f32_e32 v7, 0x40e00000, v7
	v_mul_f32_e32 v12, 0x3fd9db23, v7
	v_mul_f32_e32 v12, 0xbfb8aa3b, v12
	v_exp_f32_e32 v12, v12
	v_add_f32_e32 v14, 1.0, v14
	v_rcp_f32_e32 v14, v14
	v_fmamk_f32 v4, v68, 0x3d000000, v4
	v_add_f32_e32 v12, 1.0, v12
	v_med3_f32 v4, v4, s76, v225
	v_fmac_f32_e32 v9, 0x3d000000, v77
	v_rcp_f32_e32 v12, v12
	v_mul_f32_e32 v8, v8, v14
	v_add_f32_e32 v4, 1.0, v4
	v_fmac_f32_e32 v13, 0x3d000000, v81
	v_min_f32_e32 v9, 0x40e00000, v9
	v_mul_f32_e32 v4, v4, v8
	v_min_f32_e32 v8, 0x40e00000, v13
	v_mul_f32_e32 v13, 0x3fd9db23, v9
	v_mul_f32_e32 v13, 0xbfb8aa3b, v13
	v_exp_f32_e32 v13, v13
	v_mul_f32_e32 v7, v7, v12
	v_mul_f32_e32 v12, 0x3fd9db23, v8
	v_mul_f32_e32 v12, 0xbfb8aa3b, v12
	v_exp_f32_e32 v12, v12
	v_add_f32_e32 v13, 1.0, v13
	v_rcp_f32_e32 v13, v13
	v_med3_f32 v11, v11, s76, v225
	v_add_f32_e32 v11, 1.0, v11
	v_fmac_f32_e32 v5, 0x3d000000, v69
	v_add_f32_e32 v12, 1.0, v12
	v_mul_f32_e32 v6, v11, v6
	v_fmamk_f32 v11, v72, 0x3d000000, v16
	v_rcp_f32_e32 v12, v12
	v_med3_f32 v5, v5, s76, v225
	v_med3_f32 v25, v25, s77, v226
	v_med3_f32 v27, v27, s77, v226
	v_med3_f32 v11, v11, s76, v225
	v_mul_f32_e32 v9, v9, v13
	v_add_f32_e32 v5, 1.0, v5
	v_cvt_pk_fp8_f32 v22, v25, v27 op_sel:[0,0,1]
	v_add_f32_e32 v11, 1.0, v11
	v_fmac_f32_e32 v17, 0x3d000000, v73
	v_mul_f32_e32 v5, v5, v9
	v_med3_f32 v9, v10, s77, v226
	v_med3_f32 v6, v6, s77, v226
	v_mov_b32_e32 v24, v201
	v_med3_f32 v2, v2, s77, v226
	v_med3_f32 v3, v3, s77, v226
	v_mov_b32_e32 v25, v201
	v_mul_f32_e32 v7, v11, v7
	v_med3_f32 v11, v17, s76, v225
	v_cvt_pk_fp8_f32 v24, v9, v6
	v_cvt_pk_fp8_f32 v25, v2, v3
	v_mul_f32_e32 v8, v8, v12
	v_add_f32_e32 v11, 1.0, v11
	v_mul_f32_e32 v8, v11, v8
	v_med3_f32 v7, v7, s77, v226
	v_med3_f32 v8, v8, s77, v226
	v_med3_f32 v2, v4, s77, v226
	v_med3_f32 v3, v5, s77, v226
	v_cvt_pk_fp8_f32 v24, v7, v8 op_sel:[0,0,1]
	v_cvt_pk_fp8_f32 v25, v2, v3 op_sel:[0,0,1]
	v_add_u32_e32 v2, 0xa0, v20
	v_ashrrev_i32_e32 v3, 31, v2
	v_lshlrev_b64 v[2:3], 11, v[2:3]
	v_lshl_add_u64 v[2:3], s[16:17], 0, v[2:3]
	v_permlane16_swap_b32_e32 v22, v24
	v_permlane16_swap_b32_e32 v23, v25
	v_lshl_add_u64 v[2:3], v[2:3], 0, v[18:19]
	global_store_dwordx4 v[2:3], v[22:25], off
	s_cbranch_vccnz .LBB0_1302
	s_branch .LBB0_1301

; #define PG8_BAR __builtin_amdgcn_s_barrier()
;     __device__ __forceinline__ int krot(const Unit& u, int nt) const { return (2 * u.rb + u.pn) % nt; }
;     ...
;         rotn = has_next ? S.krot(nxt, nt) : rotc;
;         const bool full = !HALFU || cur.nvalid > 128;
; #pragma unroll 1
;         for (int t = 0; t < nt; t += 2) {
;             const bool last = (t == nt - 2);
;             const bool fin = last && !has_next;
;             const char* a1 = cA + PG8_KOFS(rotc, t + 1);
;             const size_t k2 = last ? PG8_KOFS(rotn, 0) : PG8_KOFS(rotc, t + 2), k3 = last ? PG8_KOFS(rotn, 1) : PG8_KOFS(rotc, t + 3);
;             const char* a2 = (last ? nA : cA) + k2; const char* b2 = (last ? nB : cB) + k2;
;             const char* a3 = (last ? nA : cA) + k3; const char* b3 = (last ? nB : cB) + k3;
;             unsigned o2[2][2];
; #pragma unroll
;             for (int h = 0; h < 2; ++h)
; #pragma unroll
;                 for (int i = 0; i < 2; ++i) o2[h][i] = gcur[h][i];
;     ...
; #pragma unroll
;         for (int a = 0; a < 2; ++a)
; #pragma unroll
;             for (int b = 0; b < 2; ++b)
; #pragma unroll
;                 for (int m = 0; m < 4; ++m)
; #pragma unroll
;                     for (int n = 0; n < 2; ++n) acc[a][b][m][n] = (f32x4){0.f, 0.f, 0.f, 0.f};
;         cur = nxt; cA = nA; cB = nB; rotc = rotn; ++ui;
; #pragma unroll
;         for (int h = 0; h < 2; ++h)
; #pragma unroll
;             for (int i = 0; i < 2; ++i) gcur[h][i] = gnxt[h][i];
;         if (wr == 1) PG8_BAR;
.LBB0_1411:
	s_ashr_i32 s25, s24, 31
	s_lshl_b64 s[8:9], s[24:25], 19
	s_add_u32 s28, s48, s8
	s_addc_u32 s29, s49, s9
	s_and_b64 s[8:9], s[46:47], exec
	s_cselect_b32 s23, s29, s41
	s_cselect_b32 s25, s28, s40
	s_lshl_b32 s8, s85, 1
	s_add_i32 s8, s22, s8
	s_ashr_i32 s9, s8, 31
	s_lshr_b32 s9, s9, 28
	s_add_i32 s9, s8, s9
	s_and_b32 s9, s9, -16
	s_sub_i32 s21, s8, s9
	s_and_b64 s[8:9], s[46:47], exec
	s_cselect_b32 s54, s21, s44
	s_cmpk_gt_i32 s87, 0x80
	s_cselect_b64 s[56:57], -1, 0
	s_ashr_i32 s55, s54, 31
	s_lshl_b64 s[8:9], s[54:55], 7
	s_add_u32 s8, s8, 0x80
	s_addc_u32 s9, s9, 0
	v_mov_b32_e32 v122, v205
	v_mov_b32_e32 v123, v205
	v_mov_b32_e32 v124, v205
	v_mov_b32_e32 v125, v205
	s_cmp_lt_i32 s54, 15
	v_mov_b32_e32 v98, 0
	v_mov_b64_e32 v[136:137], v[124:125]
	v_mov_b64_e32 v[140:141], v[124:125]
	v_mov_b64_e32 v[144:145], v[124:125]
	v_mov_b64_e32 v[148:149], v[124:125]
	v_mov_b64_e32 v[152:153], v[124:125]
	v_mov_b64_e32 v[156:157], v[124:125]
	v_mov_b64_e32 v[160:161], v[124:125]
	v_mov_b64_e32 v[94:95], v[122:123]
	v_mov_b64_e32 v[90:91], v[122:123]
	v_mov_b64_e32 v[86:87], v[122:123]
	v_mov_b64_e32 v[82:83], v[122:123]
	v_mov_b64_e32 v[78:79], v[122:123]
	v_mov_b64_e32 v[74:75], v[122:123]
	v_mov_b64_e32 v[70:71], v[122:123]
	v_mov_b64_e32 v[66:67], v[122:123]
	s_cselect_b32 s31, s9, 0
	s_cselect_b32 s37, s8, 0
	s_mov_b32 s55, -2
	v_cndmask_b32_e64 v217, 0, 1, s[56:57]
	v_mov_b64_e32 v[134:135], v[122:123]
	v_mov_b64_e32 v[138:139], v[122:123]
	v_mov_b64_e32 v[142:143], v[122:123]
	v_mov_b64_e32 v[146:147], v[122:123]
	v_mov_b64_e32 v[150:151], v[122:123]
	v_mov_b64_e32 v[154:155], v[122:123]
	v_mov_b64_e32 v[158:159], v[122:123]
	v_mov_b64_e32 v[96:97], v[124:125]
	v_mov_b64_e32 v[92:93], v[124:125]
	v_mov_b64_e32 v[88:89], v[124:125]
	v_mov_b64_e32 v[84:85], v[124:125]
	v_mov_b64_e32 v[80:81], v[124:125]
	v_mov_b64_e32 v[76:77], v[124:125]
	v_mov_b64_e32 v[72:73], v[124:125]
	v_mov_b64_e32 v[68:69], v[124:125]
	v_mov_b32_e32 v99, v98
	v_mov_b32_e32 v100, v98
	v_mov_b32_e32 v101, v98
	v_mov_b32_e32 v102, v98
	v_mov_b32_e32 v103, v98
	v_mov_b32_e32 v104, v98
	v_mov_b32_e32 v105, v98
	v_mov_b32_e32 v106, v98
	v_mov_b32_e32 v107, v98
	v_mov_b32_e32 v108, v98
	v_mov_b32_e32 v109, v98
	v_mov_b32_e32 v110, v98
	v_mov_b32_e32 v111, v98
	v_mov_b32_e32 v112, v98
	v_mov_b32_e32 v113, v98
	v_mov_b32_e32 v114, v98
	v_mov_b32_e32 v115, v98
	v_mov_b32_e32 v116, v98
	v_mov_b32_e32 v117, v98
	v_mov_b32_e32 v118, v98
	v_mov_b32_e32 v119, v98
	v_mov_b32_e32 v120, v98
	v_mov_b32_e32 v121, v98
	v_mov_b32_e32 v126, v98
	v_mov_b32_e32 v127, v98
	v_mov_b32_e32 v128, v98
	v_mov_b32_e32 v129, v98
	v_mov_b32_e32 v130, v98
	v_mov_b32_e32 v131, v98
	v_mov_b32_e32 v132, v98
	v_mov_b32_e32 v133, v98
	v_mov_b32_e32 v162, v98
	v_mov_b32_e32 v163, v98
	v_mov_b32_e32 v164, v98
	v_mov_b32_e32 v165, v98
	v_mov_b32_e32 v166, v98
	v_mov_b32_e32 v167, v98
	v_mov_b32_e32 v168, v98
	v_mov_b32_e32 v169, v98
	v_mov_b32_e32 v170, v98
	v_mov_b32_e32 v171, v98
	v_mov_b32_e32 v172, v98
	v_mov_b32_e32 v173, v98
	v_mov_b32_e32 v174, v98
	v_mov_b32_e32 v175, v98
	v_mov_b32_e32 v176, v98
	v_mov_b32_e32 v177, v98
	v_mov_b32_e32 v178, v98
	v_mov_b32_e32 v179, v98
	v_mov_b32_e32 v180, v98
	v_mov_b32_e32 v181, v98
	v_mov_b32_e32 v182, v98
	v_mov_b32_e32 v183, v98
	v_mov_b32_e32 v184, v98
	v_mov_b32_e32 v185, v98
	v_mov_b32_e32 v186, v98
	v_mov_b32_e32 v187, v98
	v_mov_b32_e32 v188, v98
	v_mov_b32_e32 v189, v98
	v_mov_b32_e32 v190, v98
	v_mov_b32_e32 v191, v98
	v_mov_b32_e32 v192, v98
	v_mov_b32_e32 v193, v98
	s_cmp_lt_u32 s72, 2
	s_cbranch_scc1 .Lp10_noR
	s_and_b64 vcc, exec, s[2:3]
	s_cbranch_vccz .Lp10_noR
	s_barrier
.Lp10_noR:
	s_branch .LBB0_1413
.LBB0_1412:
	s_barrier
	s_add_i32 s55, s55, 2
	s_cmp_gt_u32 s55, 13
	s_cbranch_scc1 .LBB0_1431

; #define EPI_ALD16(dst_, ptr_) asm volatile("global_load_dwordx4 %0, %1, off" : "=v"(dst_) : "v"(ptr_))
;     __device__ __forceinline__ void operator()(EPI_ARGS) const {
;         const float* bb = b2 + (size_t)u.e * D; const float* lw = lwt + (size_t)u.e * LCAP + u.rb * 256;
;         float wg[2][4]; f32x4 cb[2][2];
; #pragma unroll
;         for (int ai = 0; ai < 2; ++ai)
; #pragma unroll
;             for (int m = 0; m < 4; ++m) { const float* p_ = lw + (ai * 128 + wr * 64 + m * 16 + fr); asm volatile("global_load_dword %0, %1, off" : "=v"(wg[ai][m]) : "v"(p_)); }
; #pragma unroll
;         for (int bj = 0; bj < 2; ++bj) { const float* p_ = bb + u.pn * 256 + bj * 128 + wc * 32 + 8 * fq; EPI_ALD16(cb[bj][0], p_); EPI_ALD16(cb[bj][1], p_ + 4); }
;         asm volatile("s_waitcnt vmcnt(0)" : "+v"(wg[0][0]), "+v"(wg[0][1]), "+v"(wg[0][2]), "+v"(wg[0][3]), "+v"(wg[1][0]), "+v"(wg[1][1]), "+v"(wg[1][2]), "+v"(wg[1][3]), "+v"(cb[0][0]), "+v"(cb[0][1]), "+v"(cb[1][0]), "+v"(cb[1][1]));
; #pragma unroll
;         for (int ai = 0; ai < 2; ++ai)
; #pragma unroll
;             for (int m = 0; m < 4; ++m) { const int r = ai * 128 + wr * 64 + m * 16 + fr; wg[ai][m] = (r < u.nvalid) ? 16.0f * wg[ai][m] : 0.0f; }
; #pragma unroll
;         for (int bj = 0; bj < 2; ++bj) { const f32x4 c0 = cb[bj][0], c1 = cb[bj][1];
;             const int colq = u.pn * 256 + bj * 128 + wc * 32 + 8 * (fq & ~1);
; #pragma unroll
;             for (int ai = 0; ai < 2; ++ai)
; #pragma unroll
;                 for (int mp = 0; mp < 2; ++mp) { unsigned px[2], py[2];
; #pragma unroll
;                     for (int h = 0; h < 2; ++h) { const int m = 2 * mp + h; const f32x4 v0 = (acc[ai][bj][m][0] * 0.03125f + c0) * wg[ai][m], v1 = (acc[ai][bj][m][1] * 0.03125f + c1) * wg[ai][m];
;                         px[h] = pk4_fp8(v0[0], v0[1], v0[2], v0[3]); py[h] = pk4_fp8(v1[0], v1[1], v1[2], v1[3]); }
;                     const u32x4 q = pair16(px[0], py[0], px[1], py[1]);
;                     const int r = ai * 128 + wr * 64 + (2 * mp + (fq & 1)) * 16 + fr;
;                     *(u32x4*)(YE + ((size_t)u.pm * 256 + r) * D + colq) = q; } }
.LBB0_1433:
	s_ashr_i32 s37, s36, 31
	s_lshl_b64 s[8:9], s[36:37], 13
	s_lshl_b64 s[14:15], s[36:37], 16
	s_add_u32 s23, s73, s14
	s_addc_u32 s25, s74, s15
	s_lshl_b32 s14, s88, 8
	s_ashr_i32 s15, s14, 31
	s_lshl_b64 s[14:15], s[14:15], 2
	s_add_u32 s14, s23, s14
	s_addc_u32 s15, s25, s15
	v_lshl_add_u64 v[2:3], s[14:15], 0, v[204:205]
	v_lshl_add_u64 v[4:5], v[2:3], 0, 64
	s_mov_b64 s[14:15], 0x80
	s_nop 15
	s_nop 15
	s_waitcnt lgkmcnt(0)
	global_load_dword v18, v[2:3], off
	global_load_dword v19, v[4:5], off
	v_lshl_add_u64 v[4:5], v[2:3], 0, s[14:15]
	s_mov_b64 s[14:15], 0xc0
	global_load_dword v20, v[4:5], off
	v_lshl_add_u64 v[4:5], v[2:3], 0, s[14:15]
	global_load_dword v21, v[4:5], off
	v_lshl_add_u64 v[4:5], v[2:3], 0, s[16:17]
	s_mov_b64 s[14:15], 0x240
	s_add_u32 s23, s10, s8
	global_load_dword v22, v[4:5], off
	v_lshl_add_u64 v[4:5], v[2:3], 0, s[14:15]
	s_mov_b64 s[14:15], 0x280
	s_addc_u32 s25, s11, s9
	s_lshl_b32 s8, s38, 8
	global_load_dword v23, v[4:5], off
	v_lshl_add_u64 v[4:5], v[2:3], 0, s[14:15]
	s_mov_b64 s[14:15], 0x2c0
	s_ashr_i32 s9, s8, 31
	v_lshl_add_u64 v[2:3], v[2:3], 0, s[14:15]
	s_lshl_b64 s[14:15], s[8:9], 2
	s_add_u32 s9, s23, s14
	s_addc_u32 s15, s25, s15
	s_add_u32 s14, s9, s83
	s_addc_u32 s15, s15, 0
	v_mov_b32_e32 v217, v205
	global_load_dword v25, v[4:5], off
	global_load_dword v27, v[2:3], off
	v_lshl_add_u64 v[2:3], s[14:15], 0, v[216:217]
	v_lshl_add_u64 v[4:5], v[2:3], 0, 16
	s_mov_b64 s[14:15], 0x210
	global_load_dwordx4 v[14:17], v[2:3], off
	global_load_dwordx4 v[10:13], v[4:5], off
	v_lshl_add_u64 v[4:5], v[2:3], 0, s[16:17]
	v_lshl_add_u64 v[2:3], v[2:3], 0, s[14:15]
	global_load_dwordx4 v[6:9], v[4:5], off
	global_load_dwordx4 v[2:5], v[2:3], off
	v_cmp_gt_i32_e32 vcc, s87, v206
	s_waitcnt vmcnt(0)
	s_ashr_i32 s31, s30, 31
	v_mul_f32_e32 v18, 0x41800000, v18
	v_cndmask_b32_e32 v32, 0, v18, vcc
	v_mul_f32_e32 v18, 0x41800000, v19
	v_cmp_gt_i32_e32 vcc, s87, v1
	v_pk_fma_f32 v[38:39], v[190:191], s[18:19], v[14:15] op_sel_hi:[1,0,1]
	v_pk_fma_f32 v[42:43], v[186:187], s[18:19], v[10:11] op_sel_hi:[1,0,1]
	v_cndmask_b32_e32 v30, 0, v18, vcc
	v_mul_f32_e32 v18, 0x41800000, v20
	v_cmp_gt_i32_e32 vcc, s87, v195
	v_pk_mul_f32 v[38:39], v[38:39], v[32:33] op_sel_hi:[1,0]
	v_pk_mul_f32 v[42:43], v[42:43], v[32:33] op_sel_hi:[1,0]
	v_cndmask_b32_e32 v28, 0, v18, vcc
	v_mul_f32_e32 v18, 0x41800000, v21
	v_med3_f32 v19, v38, s84, v229
	v_med3_f32 v21, v39, s84, v229
	v_mov_b32_e32 v38, v205
	v_cvt_pk_fp8_f32 v38, v19, v21
	v_med3_f32 v19, v42, s84, v229
	v_med3_f32 v21, v43, s84, v229
	v_mov_b32_e32 v39, v205
	v_pk_fma_f32 v[40:41], v[188:189], s[18:19], v[12:13] op_sel_hi:[1,0,1]
	v_cvt_pk_fp8_f32 v39, v19, v21
	v_pk_mul_f32 v[40:41], v[40:41], v[32:33] op_sel_hi:[1,0]
	v_pk_fma_f32 v[44:45], v[178:179], s[18:19], v[10:11] op_sel_hi:[1,0,1]
	v_med3_f32 v19, v40, s84, v229
	v_med3_f32 v21, v41, s84, v229
	v_pk_fma_f32 v[40:41], v[182:183], s[18:19], v[14:15] op_sel_hi:[1,0,1]
	v_cmp_gt_i32_e32 vcc, s87, v207
	v_pk_mul_f32 v[40:41], v[40:41], v[30:31] op_sel_hi:[1,0]
	v_cvt_pk_fp8_f32 v39, v19, v21 op_sel:[0,0,1]
	v_pk_mul_f32 v[44:45], v[44:45], v[30:31] op_sel_hi:[1,0]
	v_med3_f32 v19, v40, s84, v229
	v_med3_f32 v21, v41, s84, v229
	v_mov_b32_e32 v40, v205
	v_cndmask_b32_e32 v26, 0, v18, vcc
	v_mul_f32_e32 v18, 0x41800000, v22
	v_cmp_gt_i32_e32 vcc, s87, v218
	v_pk_fma_f32 v[36:37], v[192:193], s[18:19], v[16:17] op_sel_hi:[1,0,1]
	v_cvt_pk_fp8_f32 v40, v19, v21
	v_med3_f32 v19, v44, s84, v229
	v_med3_f32 v21, v45, s84, v229
	v_mov_b32_e32 v41, v205
	v_cndmask_b32_e32 v24, 0, v18, vcc
	v_mul_f32_e32 v18, 0x41800000, v23
	v_cmp_gt_i32_e32 vcc, s87, v219
	v_pk_mul_f32 v[36:37], v[36:37], v[32:33] op_sel_hi:[1,0]
	v_cvt_pk_fp8_f32 v41, v19, v21
	v_cndmask_b32_e32 v22, 0, v18, vcc
	v_mul_f32_e32 v18, 0x41800000, v25
	v_med3_f32 v23, v36, s84, v229
	v_med3_f32 v25, v37, s84, v229
	v_pk_fma_f32 v[36:37], v[184:185], s[18:19], v[16:17] op_sel_hi:[1,0,1]
	v_pk_fma_f32 v[42:43], v[180:181], s[18:19], v[12:13] op_sel_hi:[1,0,1]
	v_pk_mul_f32 v[36:37], v[36:37], v[30:31] op_sel_hi:[1,0]
	v_pk_mul_f32 v[42:43], v[42:43], v[30:31] op_sel_hi:[1,0]
	v_cvt_pk_fp8_f32 v38, v23, v25 op_sel:[0,0,1]
	v_med3_f32 v23, v36, s84, v229
	v_med3_f32 v25, v37, s84, v229
	v_med3_f32 v19, v42, s84, v229
	v_med3_f32 v21, v43, s84, v229
	v_or_b32_e32 v34, s8, v222
	v_cvt_pk_fp8_f32 v40, v23, v25 op_sel:[0,0,1]
	v_cvt_pk_fp8_f32 v41, v19, v21 op_sel:[0,0,1]
	s_lshl_b64 s[8:9], s[30:31], 19
	s_add_u32 s8, s75, s8
	s_addc_u32 s9, s76, s9
	v_ashrrev_i32_e32 v35, 31, v34
	v_lshl_add_u64 v[36:37], s[8:9], 0, v[208:209]
	v_permlane16_swap_b32_e32 v38, v40
	v_permlane16_swap_b32_e32 v39, v41
	v_lshl_add_u64 v[36:37], v[36:37], 0, v[34:35]
	global_store_dwordx4 v[36:37], v[38:41], off
	v_pk_fma_f32 v[44:45], v[170:171], s[18:19], v[10:11] op_sel_hi:[1,0,1]
	v_pk_fma_f32 v[42:43], v[172:173], s[18:19], v[12:13] op_sel_hi:[1,0,1]
	v_pk_fma_f32 v[40:41], v[174:175], s[18:19], v[14:15] op_sel_hi:[1,0,1]
	v_pk_mul_f32 v[44:45], v[44:45], v[28:29] op_sel_hi:[1,0]
	v_pk_mul_f32 v[40:41], v[40:41], v[28:29] op_sel_hi:[1,0]
	v_pk_mul_f32 v[42:43], v[42:43], v[28:29] op_sel_hi:[1,0]
	v_med3_f32 v19, v40, s84, v229
	v_med3_f32 v21, v41, s84, v229
	v_mov_b32_e32 v40, v205
	v_cvt_pk_fp8_f32 v40, v19, v21
	v_med3_f32 v19, v44, s84, v229
	v_med3_f32 v21, v45, s84, v229
	v_mov_b32_e32 v41, v205
	v_cvt_pk_fp8_f32 v41, v19, v21
	v_med3_f32 v19, v42, s84, v229
	v_med3_f32 v21, v43, s84, v229
	v_pk_fma_f32 v[42:43], v[166:167], s[18:19], v[14:15] op_sel_hi:[1,0,1]
	v_pk_fma_f32 v[46:47], v[162:163], s[18:19], v[10:11] op_sel_hi:[1,0,1]
;     __device__ __forceinline__ void operator()(EPI_ARGS) const {
;     ...
; #pragma unroll
;         for (int bj = 0; bj < 2; ++bj) { const f32x4 c0 = cb[bj][0], c1 = cb[bj][1];
;             const int colq = u.pn * 256 + bj * 128 + wc * 32 + 8 * (fq & ~1);
; #pragma unroll
;             for (int ai = 0; ai < 2; ++ai)
; #pragma unroll
;                 for (int mp = 0; mp < 2; ++mp) { unsigned px[2], py[2];
; #pragma unroll
;                     for (int h = 0; h < 2; ++h) { const int m = 2 * mp + h; const f32x4 v0 = (acc[ai][bj][m][0] * 0.03125f + c0) * wg[ai][m], v1 = (acc[ai][bj][m][1] * 0.03125f + c1) * wg[ai][m];
;                         px[h] = pk4_fp8(v0[0], v0[1], v0[2], v0[3]); py[h] = pk4_fp8(v1[0], v1[1], v1[2], v1[3]); }
;                     const u32x4 q = pair16(px[0], py[0], px[1], py[1]);
;                     const int r = ai * 128 + wr * 64 + (2 * mp + (fq & 1)) * 16 + fr;
;                     *(u32x4*)(YE + ((size_t)u.pm * 256 + r) * D + colq) = q; } }
	v_pk_mul_f32 v[42:43], v[42:43], v[26:27] op_sel_hi:[1,0]
	v_cvt_pk_fp8_f32 v41, v19, v21 op_sel:[0,0,1]
	v_pk_mul_f32 v[46:47], v[46:47], v[26:27] op_sel_hi:[1,0]
	v_med3_f32 v19, v42, s84, v229
	v_med3_f32 v21, v43, s84, v229
	v_mov_b32_e32 v42, v205
	v_pk_fma_f32 v[38:39], v[176:177], s[18:19], v[16:17] op_sel_hi:[1,0,1]
	v_cvt_pk_fp8_f32 v42, v19, v21
	v_med3_f32 v19, v46, s84, v229
	v_med3_f32 v21, v47, s84, v229
	v_mov_b32_e32 v43, v205
	v_pk_mul_f32 v[38:39], v[38:39], v[28:29] op_sel_hi:[1,0]
	v_cvt_pk_fp8_f32 v43, v19, v21
	v_med3_f32 v23, v38, s84, v229
	v_med3_f32 v25, v39, s84, v229
	v_pk_fma_f32 v[38:39], v[168:169], s[18:19], v[16:17] op_sel_hi:[1,0,1]
	v_pk_fma_f32 v[44:45], v[164:165], s[18:19], v[12:13] op_sel_hi:[1,0,1]
	v_pk_mul_f32 v[38:39], v[38:39], v[26:27] op_sel_hi:[1,0]
	v_pk_mul_f32 v[44:45], v[44:45], v[26:27] op_sel_hi:[1,0]
	v_cvt_pk_fp8_f32 v40, v23, v25 op_sel:[0,0,1]
	v_med3_f32 v23, v38, s84, v229
	v_med3_f32 v25, v39, s84, v229
	v_med3_f32 v19, v44, s84, v229
	v_med3_f32 v21, v45, s84, v229
	v_cvt_pk_fp8_f32 v42, v23, v25 op_sel:[0,0,1]
	v_cvt_pk_fp8_f32 v43, v19, v21 op_sel:[0,0,1]
	v_lshl_add_u64 v[38:39], s[8:9], 0, v[210:211]
	v_lshl_add_u64 v[38:39], v[38:39], 0, v[34:35]
	v_permlane16_swap_b32_e32 v40, v42
	v_permlane16_swap_b32_e32 v41, v43
	global_store_dwordx4 v[38:39], v[40:43], off
	v_pk_fma_f32 v[46:47], v[154:155], s[18:19], v[10:11] op_sel_hi:[1,0,1]
	v_pk_fma_f32 v[44:45], v[156:157], s[18:19], v[12:13] op_sel_hi:[1,0,1]
	v_pk_fma_f32 v[42:43], v[158:159], s[18:19], v[14:15] op_sel_hi:[1,0,1]
	v_pk_mul_f32 v[46:47], v[46:47], v[24:25] op_sel_hi:[1,0]
	v_pk_mul_f32 v[42:43], v[42:43], v[24:25] op_sel_hi:[1,0]
	v_pk_fma_f32 v[40:41], v[160:161], s[18:19], v[16:17] op_sel_hi:[1,0,1]
	v_med3_f32 v19, v42, s84, v229
	v_med3_f32 v21, v43, s84, v229
	v_mov_b32_e32 v42, v205
	v_cvt_pk_fp8_f32 v42, v19, v21
	v_med3_f32 v19, v46, s84, v229
	v_med3_f32 v21, v47, s84, v229
	v_mov_b32_e32 v43, v205
	v_cvt_pk_fp8_f32 v43, v19, v21
	v_pk_mul_f32 v[40:41], v[40:41], v[24:25] op_sel_hi:[1,0]
	v_pk_mul_f32 v[44:45], v[44:45], v[24:25] op_sel_hi:[1,0]
	v_med3_f32 v23, v40, s84, v229
	v_med3_f32 v19, v44, s84, v229
	v_med3_f32 v21, v45, s84, v229
	v_pk_fma_f32 v[44:45], v[150:151], s[18:19], v[14:15] op_sel_hi:[1,0,1]
	v_pk_fma_f32 v[48:49], v[146:147], s[18:19], v[10:11] op_sel_hi:[1,0,1]
	v_pk_mul_f32 v[44:45], v[44:45], v[22:23] op_sel_hi:[1,0]
	v_cvt_pk_fp8_f32 v43, v19, v21 op_sel:[0,0,1]
	v_pk_mul_f32 v[48:49], v[48:49], v[22:23] op_sel_hi:[1,0]
	v_med3_f32 v19, v44, s84, v229
	v_med3_f32 v21, v45, s84, v229
	v_mov_b32_e32 v44, v205
	v_cvt_pk_fp8_f32 v44, v19, v21
	v_med3_f32 v19, v48, s84, v229
	v_med3_f32 v21, v49, s84, v229
	v_mov_b32_e32 v45, v205
	v_cvt_pk_fp8_f32 v45, v19, v21
	v_med3_f32 v25, v41, s84, v229
	v_pk_fma_f32 v[40:41], v[152:153], s[18:19], v[16:17] op_sel_hi:[1,0,1]
	v_pk_fma_f32 v[46:47], v[148:149], s[18:19], v[12:13] op_sel_hi:[1,0,1]
	v_pk_mul_f32 v[40:41], v[40:41], v[22:23] op_sel_hi:[1,0]
	v_pk_mul_f32 v[46:47], v[46:47], v[22:23] op_sel_hi:[1,0]
	v_cvt_pk_fp8_f32 v42, v23, v25 op_sel:[0,0,1]
	v_med3_f32 v23, v40, s84, v229
	v_med3_f32 v25, v41, s84, v229
	v_med3_f32 v19, v46, s84, v229
	v_med3_f32 v21, v47, s84, v229
	v_cvt_pk_fp8_f32 v44, v23, v25 op_sel:[0,0,1]
	v_cvt_pk_fp8_f32 v45, v19, v21 op_sel:[0,0,1]
	v_lshl_add_u64 v[40:41], s[8:9], 0, v[212:213]
	v_cmp_gt_i32_e32 vcc, s87, v220
	v_permlane16_swap_b32_e32 v42, v44
	v_permlane16_swap_b32_e32 v43, v45
	v_lshl_add_u64 v[40:41], v[40:41], 0, v[34:35]
	v_cndmask_b32_e32 v20, 0, v18, vcc
	global_store_dwordx4 v[40:41], v[42:45], off
	v_pk_fma_f32 v[46:47], v[140:141], s[18:19], v[12:13] op_sel_hi:[1,0,1]
	v_pk_fma_f32 v[48:49], v[138:139], s[18:19], v[10:11] op_sel_hi:[1,0,1]
	v_pk_fma_f32 v[42:43], v[144:145], s[18:19], v[16:17] op_sel_hi:[1,0,1]
	v_pk_fma_f32 v[44:45], v[142:143], s[18:19], v[14:15] op_sel_hi:[1,0,1]
	v_pk_mul_f32 v[42:43], v[42:43], v[20:21] op_sel_hi:[1,0]
	v_pk_mul_f32 v[44:45], v[44:45], v[20:21] op_sel_hi:[1,0]
	v_pk_mul_f32 v[46:47], v[46:47], v[20:21] op_sel_hi:[1,0]
	v_pk_mul_f32 v[48:49], v[48:49], v[20:21] op_sel_hi:[1,0]
	v_med3_f32 v19, v44, s84, v229
	v_med3_f32 v21, v45, s84, v229
	v_med3_f32 v23, v42, s84, v229
	v_mov_b32_e32 v42, v205
	v_mul_f32_e32 v18, 0x41800000, v27
	v_cmp_gt_i32_e32 vcc, s87, v221
	v_med3_f32 v25, v43, s84, v229
	v_cvt_pk_fp8_f32 v42, v19, v21
	v_med3_f32 v19, v48, s84, v229
	v_med3_f32 v21, v49, s84, v229
	v_mov_b32_e32 v43, v205
	v_cndmask_b32_e32 v18, 0, v18, vcc
	v_cvt_pk_fp8_f32 v43, v19, v21
	v_med3_f32 v19, v46, s84, v229
	v_pk_fma_f32 v[10:11], v[122:123], s[18:19], v[10:11] op_sel_hi:[1,0,1]
	v_pk_fma_f32 v[14:15], v[134:135], s[18:19], v[14:15] op_sel_hi:[1,0,1]
	v_pk_mul_f32 v[10:11], v[10:11], v[18:19] op_sel_hi:[1,0]
	v_pk_mul_f32 v[14:15], v[14:15], v[18:19] op_sel_hi:[1,0]
	v_med3_f32 v10, v10, s84, v229
	v_med3_f32 v11, v11, s84, v229
	v_mov_b32_e32 v45, v205
	v_med3_f32 v14, v14, s84, v229
	v_med3_f32 v15, v15, s84, v229
	v_mov_b32_e32 v44, v205
	v_cvt_pk_fp8_f32 v45, v10, v11
	v_pk_fma_f32 v[12:13], v[124:125], s[18:19], v[12:13] op_sel_hi:[1,0,1]
	v_cvt_pk_fp8_f32 v44, v14, v15
	v_pk_fma_f32 v[16:17], v[136:137], s[18:19], v[16:17] op_sel_hi:[1,0,1]
	v_pk_mul_f32 v[12:13], v[12:13], v[18:19] op_sel_hi:[1,0]
	v_pk_mul_f32 v[16:17], v[16:17], v[18:19] op_sel_hi:[1,0]
	v_med3_f32 v10, v12, s84, v229
	v_med3_f32 v11, v13, s84, v229
	v_med3_f32 v16, v16, s84, v229
	v_med3_f32 v17, v17, s84, v229
	v_cvt_pk_fp8_f32 v45, v10, v11 op_sel:[0,0,1]
	v_lshl_add_u64 v[10:11], s[8:9], 0, v[214:215]
	v_pk_fma_f32 v[12:13], v[132:133], s[18:19], v[8:9] op_sel_hi:[1,0,1]
;     __device__ __forceinline__ void operator()(EPI_ARGS) const {
;     ...
; #pragma unroll
;         for (int bj = 0; bj < 2; ++bj) { const f32x4 c0 = cb[bj][0], c1 = cb[bj][1];
;             const int colq = u.pn * 256 + bj * 128 + wc * 32 + 8 * (fq & ~1);
; #pragma unroll
;             for (int ai = 0; ai < 2; ++ai)
; #pragma unroll
;                 for (int mp = 0; mp < 2; ++mp) { unsigned px[2], py[2];
; #pragma unroll
;                     for (int h = 0; h < 2; ++h) { const int m = 2 * mp + h; const f32x4 v0 = (acc[ai][bj][m][0] * 0.03125f + c0) * wg[ai][m], v1 = (acc[ai][bj][m][1] * 0.03125f + c1) * wg[ai][m];
;                         px[h] = pk4_fp8(v0[0], v0[1], v0[2], v0[3]); py[h] = pk4_fp8(v1[0], v1[1], v1[2], v1[3]); }
;                     const u32x4 q = pair16(px[0], py[0], px[1], py[1]);
;                     const int r = ai * 128 + wr * 64 + (2 * mp + (fq & 1)) * 16 + fr;
;                     *(u32x4*)(YE + ((size_t)u.pm * 256 + r) * D + colq) = q; } }
	v_pk_fma_f32 v[14:15], v[130:131], s[18:19], v[6:7] op_sel_hi:[1,0,1]
	v_med3_f32 v21, v47, s84, v229
	v_cvt_pk_fp8_f32 v44, v16, v17 op_sel:[0,0,1]
	v_lshl_add_u64 v[10:11], v[10:11], 0, v[34:35]
	v_pk_mul_f32 v[12:13], v[12:13], v[32:33] op_sel_hi:[1,0]
	v_pk_mul_f32 v[14:15], v[14:15], v[32:33] op_sel_hi:[1,0]
	v_pk_fma_f32 v[16:17], v[128:129], s[18:19], v[4:5] op_sel_hi:[1,0,1]
	v_pk_fma_f32 v[34:35], v[126:127], s[18:19], v[2:3] op_sel_hi:[1,0,1]
	v_cvt_pk_fp8_f32 v43, v19, v21 op_sel:[0,0,1]
	v_pk_mul_f32 v[16:17], v[16:17], v[32:33] op_sel_hi:[1,0]
	v_pk_mul_f32 v[32:33], v[34:35], v[32:33] op_sel_hi:[1,0]
	v_med3_f32 v14, v14, s84, v229
	v_med3_f32 v15, v15, s84, v229
	v_med3_f32 v19, v12, s84, v229
	v_mov_b32_e32 v12, v205
	v_med3_f32 v21, v13, s84, v229
	v_cvt_pk_fp8_f32 v12, v14, v15
	v_med3_f32 v14, v32, s84, v229
	v_med3_f32 v15, v33, s84, v229
	v_mov_b32_e32 v13, v205
	v_cvt_pk_fp8_f32 v13, v14, v15
	v_med3_f32 v14, v16, s84, v229
	v_med3_f32 v15, v17, s84, v229
	v_pk_fma_f32 v[16:17], v[118:119], s[18:19], v[6:7] op_sel_hi:[1,0,1]
	v_cvt_pk_fp8_f32 v13, v14, v15 op_sel:[0,0,1]
	v_pk_fma_f32 v[14:15], v[120:121], s[18:19], v[8:9] op_sel_hi:[1,0,1]
	v_pk_mul_f32 v[16:17], v[16:17], v[30:31] op_sel_hi:[1,0]
	v_pk_mul_f32 v[14:15], v[14:15], v[30:31] op_sel_hi:[1,0]
	v_pk_fma_f32 v[32:33], v[116:117], s[18:19], v[4:5] op_sel_hi:[1,0,1]
	v_pk_fma_f32 v[34:35], v[114:115], s[18:19], v[2:3] op_sel_hi:[1,0,1]
	v_cvt_pk_fp8_f32 v12, v19, v21 op_sel:[0,0,1]
	v_pk_mul_f32 v[32:33], v[32:33], v[30:31] op_sel_hi:[1,0]
	v_pk_mul_f32 v[30:31], v[34:35], v[30:31] op_sel_hi:[1,0]
	v_med3_f32 v16, v16, s84, v229
	v_med3_f32 v17, v17, s84, v229
	v_med3_f32 v19, v14, s84, v229
	v_mov_b32_e32 v14, v205
	v_med3_f32 v21, v15, s84, v229
	v_cvt_pk_fp8_f32 v14, v16, v17
	v_med3_f32 v16, v30, s84, v229
	v_med3_f32 v17, v31, s84, v229
	v_mov_b32_e32 v15, v205
	v_cvt_pk_fp8_f32 v15, v16, v17
	v_med3_f32 v16, v32, s84, v229
	v_med3_f32 v17, v33, s84, v229
	v_cvt_pk_fp8_f32 v14, v19, v21 op_sel:[0,0,1]
	v_cvt_pk_fp8_f32 v15, v16, v17 op_sel:[0,0,1]
	v_pk_fma_f32 v[16:17], v[108:109], s[18:19], v[4:5] op_sel_hi:[1,0,1]
	v_pk_fma_f32 v[30:31], v[106:107], s[18:19], v[2:3] op_sel_hi:[1,0,1]
	v_permlane16_swap_b32_e32 v12, v14
	v_permlane16_swap_b32_e32 v13, v15
	global_store_dwordx4 v[36:37], v[12:15], off offset:128
	v_pk_mul_f32 v[16:17], v[16:17], v[28:29] op_sel_hi:[1,0]
	v_cvt_pk_fp8_f32 v42, v23, v25 op_sel:[0,0,1]
	v_pk_fma_f32 v[12:13], v[112:113], s[18:19], v[8:9] op_sel_hi:[1,0,1]
	v_pk_fma_f32 v[14:15], v[110:111], s[18:19], v[6:7] op_sel_hi:[1,0,1]
	v_pk_mul_f32 v[12:13], v[12:13], v[28:29] op_sel_hi:[1,0]
	v_pk_mul_f32 v[14:15], v[14:15], v[28:29] op_sel_hi:[1,0]
	v_pk_mul_f32 v[28:29], v[30:31], v[28:29] op_sel_hi:[1,0]
	v_med3_f32 v14, v14, s84, v229
	v_med3_f32 v15, v15, s84, v229
	v_med3_f32 v19, v12, s84, v229
	v_mov_b32_e32 v12, v205
	v_med3_f32 v21, v13, s84, v229
	v_cvt_pk_fp8_f32 v12, v14, v15
	v_med3_f32 v14, v28, s84, v229
	v_med3_f32 v15, v29, s84, v229
	v_mov_b32_e32 v13, v205
	v_cvt_pk_fp8_f32 v13, v14, v15
	v_med3_f32 v14, v16, s84, v229
	v_med3_f32 v15, v17, s84, v229
	v_pk_fma_f32 v[16:17], v[102:103], s[18:19], v[6:7] op_sel_hi:[1,0,1]
	v_cvt_pk_fp8_f32 v13, v14, v15 op_sel:[0,0,1]
	v_pk_fma_f32 v[14:15], v[104:105], s[18:19], v[8:9] op_sel_hi:[1,0,1]
	v_pk_mul_f32 v[16:17], v[16:17], v[26:27] op_sel_hi:[1,0]
	v_pk_mul_f32 v[14:15], v[14:15], v[26:27] op_sel_hi:[1,0]
	v_pk_fma_f32 v[28:29], v[100:101], s[18:19], v[4:5] op_sel_hi:[1,0,1]
	v_pk_fma_f32 v[30:31], v[98:99], s[18:19], v[2:3] op_sel_hi:[1,0,1]
	v_cvt_pk_fp8_f32 v12, v19, v21 op_sel:[0,0,1]
	v_pk_mul_f32 v[28:29], v[28:29], v[26:27] op_sel_hi:[1,0]
	v_pk_mul_f32 v[26:27], v[30:31], v[26:27] op_sel_hi:[1,0]
	v_med3_f32 v16, v16, s84, v229
	v_med3_f32 v17, v17, s84, v229
	v_med3_f32 v19, v14, s84, v229
	v_mov_b32_e32 v14, v205
	v_med3_f32 v21, v15, s84, v229
	v_cvt_pk_fp8_f32 v14, v16, v17
	v_med3_f32 v16, v26, s84, v229
	v_med3_f32 v17, v27, s84, v229
	v_mov_b32_e32 v15, v205
	v_cvt_pk_fp8_f32 v15, v16, v17
	v_med3_f32 v16, v28, s84, v229
	v_med3_f32 v17, v29, s84, v229
	v_cvt_pk_fp8_f32 v14, v19, v21 op_sel:[0,0,1]
	v_cvt_pk_fp8_f32 v15, v16, v17 op_sel:[0,0,1]
	v_pk_fma_f32 v[16:17], v[92:93], s[18:19], v[4:5] op_sel_hi:[1,0,1]
	v_pk_fma_f32 v[26:27], v[90:91], s[18:19], v[2:3] op_sel_hi:[1,0,1]
; #define PG8_BAR __builtin_amdgcn_s_barrier()
;     ...
;         if (!has_next) break;
; #pragma unroll
;         for (int a = 0; a < 2; ++a)
; #pragma unroll
;             for (int b = 0; b < 2; ++b)
; #pragma unroll
;                 for (int m = 0; m < 4; ++m)
; #pragma unroll
;                     for (int n = 0; n < 2; ++n) acc[a][b][m][n] = (f32x4){0.f, 0.f, 0.f, 0.f};
;         cur = nxt; cA = nA; cB = nB; rotc = rotn; ++ui;
; #pragma unroll
;         for (int h = 0; h < 2; ++h)
; #pragma unroll
;             for (int i = 0; i < 2; ++i) gcur[h][i] = gnxt[h][i];
;         if (wr == 1) PG8_BAR;
;     }
;     __device__ __forceinline__ void operator()(EPI_ARGS) const {
;     ...
; #pragma unroll
;         for (int bj = 0; bj < 2; ++bj) { const f32x4 c0 = cb[bj][0], c1 = cb[bj][1];
;             const int colq = u.pn * 256 + bj * 128 + wc * 32 + 8 * (fq & ~1);
; #pragma unroll
;             for (int ai = 0; ai < 2; ++ai)
; #pragma unroll
;                 for (int mp = 0; mp < 2; ++mp) { unsigned px[2], py[2];
; #pragma unroll
;                     for (int h = 0; h < 2; ++h) { const int m = 2 * mp + h; const f32x4 v0 = (acc[ai][bj][m][0] * 0.03125f + c0) * wg[ai][m], v1 = (acc[ai][bj][m][1] * 0.03125f + c1) * wg[ai][m];
;                         px[h] = pk4_fp8(v0[0], v0[1], v0[2], v0[3]); py[h] = pk4_fp8(v1[0], v1[1], v1[2], v1[3]); }
;                     const u32x4 q = pair16(px[0], py[0], px[1], py[1]);
;                     const int r = ai * 128 + wr * 64 + (2 * mp + (fq & 1)) * 16 + fr;
;                     *(u32x4*)(YE + ((size_t)u.pm * 256 + r) * D + colq) = q; } }
	v_permlane16_swap_b32_e32 v12, v14
	v_permlane16_swap_b32_e32 v13, v15
	global_store_dwordx4 v[38:39], v[12:15], off offset:128
	v_pk_mul_f32 v[16:17], v[16:17], v[24:25] op_sel_hi:[1,0]
	v_permlane16_swap_b32_e32 v42, v44
	v_pk_fma_f32 v[12:13], v[96:97], s[18:19], v[8:9] op_sel_hi:[1,0,1]
	v_pk_fma_f32 v[14:15], v[94:95], s[18:19], v[6:7] op_sel_hi:[1,0,1]
	v_pk_mul_f32 v[12:13], v[12:13], v[24:25] op_sel_hi:[1,0]
	v_pk_mul_f32 v[14:15], v[14:15], v[24:25] op_sel_hi:[1,0]
	v_pk_mul_f32 v[24:25], v[26:27], v[24:25] op_sel_hi:[1,0]
	v_med3_f32 v14, v14, s84, v229
	v_med3_f32 v15, v15, s84, v229
	v_med3_f32 v19, v12, s84, v229
	v_mov_b32_e32 v12, v205
	v_med3_f32 v21, v13, s84, v229
	v_cvt_pk_fp8_f32 v12, v14, v15
	v_med3_f32 v14, v24, s84, v229
	v_med3_f32 v15, v25, s84, v229
	v_mov_b32_e32 v13, v205
	v_cvt_pk_fp8_f32 v13, v14, v15
	v_med3_f32 v14, v16, s84, v229
	v_med3_f32 v15, v17, s84, v229
	v_pk_fma_f32 v[16:17], v[86:87], s[18:19], v[6:7] op_sel_hi:[1,0,1]
	v_cvt_pk_fp8_f32 v13, v14, v15 op_sel:[0,0,1]
	v_pk_fma_f32 v[14:15], v[88:89], s[18:19], v[8:9] op_sel_hi:[1,0,1]
	v_pk_mul_f32 v[16:17], v[16:17], v[22:23] op_sel_hi:[1,0]
	v_pk_mul_f32 v[14:15], v[14:15], v[22:23] op_sel_hi:[1,0]
	v_pk_fma_f32 v[24:25], v[84:85], s[18:19], v[4:5] op_sel_hi:[1,0,1]
	v_pk_fma_f32 v[26:27], v[82:83], s[18:19], v[2:3] op_sel_hi:[1,0,1]
	v_cvt_pk_fp8_f32 v12, v19, v21 op_sel:[0,0,1]
	v_pk_mul_f32 v[24:25], v[24:25], v[22:23] op_sel_hi:[1,0]
	v_pk_mul_f32 v[22:23], v[26:27], v[22:23] op_sel_hi:[1,0]
	v_med3_f32 v16, v16, s84, v229
	v_med3_f32 v17, v17, s84, v229
	v_med3_f32 v19, v14, s84, v229
	v_mov_b32_e32 v14, v205
	v_med3_f32 v21, v15, s84, v229
	v_cvt_pk_fp8_f32 v14, v16, v17
	v_med3_f32 v16, v22, s84, v229
	v_med3_f32 v17, v23, s84, v229
	v_mov_b32_e32 v15, v205
	v_cvt_pk_fp8_f32 v15, v16, v17
	v_med3_f32 v16, v24, s84, v229
	v_med3_f32 v17, v25, s84, v229
	v_cvt_pk_fp8_f32 v14, v19, v21 op_sel:[0,0,1]
	v_cvt_pk_fp8_f32 v15, v16, v17 op_sel:[0,0,1]
	v_pk_fma_f32 v[16:17], v[76:77], s[18:19], v[4:5] op_sel_hi:[1,0,1]
	v_pk_fma_f32 v[22:23], v[74:75], s[18:19], v[2:3] op_sel_hi:[1,0,1]
	v_permlane16_swap_b32_e32 v12, v14
	v_permlane16_swap_b32_e32 v13, v15
	global_store_dwordx4 v[40:41], v[12:15], off offset:128
	v_pk_mul_f32 v[16:17], v[16:17], v[20:21] op_sel_hi:[1,0]
	v_pk_fma_f32 v[2:3], v[66:67], s[18:19], v[2:3] op_sel_hi:[1,0,1]
	v_pk_fma_f32 v[12:13], v[80:81], s[18:19], v[8:9] op_sel_hi:[1,0,1]
	v_pk_fma_f32 v[14:15], v[78:79], s[18:19], v[6:7] op_sel_hi:[1,0,1]
	v_pk_mul_f32 v[12:13], v[12:13], v[20:21] op_sel_hi:[1,0]
	v_pk_mul_f32 v[14:15], v[14:15], v[20:21] op_sel_hi:[1,0]
	v_pk_mul_f32 v[20:21], v[22:23], v[20:21] op_sel_hi:[1,0]
	v_med3_f32 v14, v14, s84, v229
	v_med3_f32 v15, v15, s84, v229
	v_med3_f32 v19, v12, s84, v229
	v_mov_b32_e32 v12, v205
	v_med3_f32 v22, v13, s84, v229
	v_cvt_pk_fp8_f32 v12, v14, v15
	v_med3_f32 v14, v20, s84, v229
	v_med3_f32 v15, v21, s84, v229
	v_mov_b32_e32 v13, v205
	v_cvt_pk_fp8_f32 v13, v14, v15
	v_pk_fma_f32 v[6:7], v[70:71], s[18:19], v[6:7] op_sel_hi:[1,0,1]
	v_med3_f32 v14, v16, s84, v229
	v_med3_f32 v15, v17, s84, v229
	v_pk_mul_f32 v[6:7], v[6:7], v[18:19] op_sel_hi:[1,0]
	v_pk_mul_f32 v[2:3], v[2:3], v[18:19] op_sel_hi:[1,0]
	v_cvt_pk_fp8_f32 v13, v14, v15 op_sel:[0,0,1]
	v_med3_f32 v6, v6, s84, v229
	v_med3_f32 v7, v7, s84, v229
	v_mov_b32_e32 v14, v205
	v_med3_f32 v2, v2, s84, v229
	v_med3_f32 v3, v3, s84, v229
	v_mov_b32_e32 v15, v205
	v_cvt_pk_fp8_f32 v14, v6, v7
	v_cvt_pk_fp8_f32 v15, v2, v3
	v_pk_fma_f32 v[8:9], v[72:73], s[18:19], v[8:9] op_sel_hi:[1,0,1]
	v_pk_fma_f32 v[4:5], v[68:69], s[18:19], v[4:5] op_sel_hi:[1,0,1]
	v_pk_mul_f32 v[8:9], v[8:9], v[18:19] op_sel_hi:[1,0]
	v_pk_mul_f32 v[4:5], v[4:5], v[18:19] op_sel_hi:[1,0]
	v_med3_f32 v8, v8, s84, v229
	v_med3_f32 v9, v9, s84, v229
	v_med3_f32 v2, v4, s84, v229
	v_med3_f32 v3, v5, s84, v229
	v_cvt_pk_fp8_f32 v12, v19, v22 op_sel:[0,0,1]
	v_cvt_pk_fp8_f32 v14, v8, v9 op_sel:[0,0,1]
	v_cvt_pk_fp8_f32 v15, v2, v3 op_sel:[0,0,1]
	v_permlane16_swap_b32_e32 v43, v45
	v_permlane16_swap_b32_e32 v12, v14
	v_permlane16_swap_b32_e32 v13, v15
	s_and_b64 vcc, exec, s[6:7]
	s_mov_b64 s[6:7], -1
	global_store_dwordx4 v[10:11], v[42:45], off
	global_store_dwordx4 v[10:11], v[12:15], off offset:128
	s_cbranch_vccnz .LBB0_1406
	s_branch .LBB0_1405

; __global__ void __launch_bounds__(NWAVES * 64, 2) fwd_kernel(Args args) {
	.amdhsa_kernel _Z10fwd_kernel4Args
		.amdhsa_group_segment_fixed_size 0
		.amdhsa_private_segment_fixed_size 0
		.amdhsa_kernarg_size 528
		.amdhsa_user_sgpr_count 2
		.amdhsa_user_sgpr_dispatch_ptr 0
		.amdhsa_user_sgpr_queue_ptr 0
		.amdhsa_user_sgpr_kernarg_segment_ptr 1
		.amdhsa_user_sgpr_dispatch_id 0
		.amdhsa_user_sgpr_kernarg_preload_length 0
		.amdhsa_user_sgpr_kernarg_preload_offset 0
		.amdhsa_user_sgpr_private_segment_size 0
		.amdhsa_uses_dynamic_stack 0
		.amdhsa_enable_private_segment 0
		.amdhsa_system_sgpr_workgroup_id_x 1
		.amdhsa_system_sgpr_workgroup_id_y 0
		.amdhsa_system_sgpr_workgroup_id_z 0
		.amdhsa_system_sgpr_workgroup_info 0
		.amdhsa_system_vgpr_workitem_id 0
		.amdhsa_next_free_vgpr 256
		.amdhsa_next_free_sgpr 102
		.amdhsa_accum_offset 256
		.amdhsa_reserve_vcc 1
		.amdhsa_float_round_mode_32 0
		.amdhsa_float_round_mode_16_64 0
		.amdhsa_float_denorm_mode_32 3
		.amdhsa_float_denorm_mode_16_64 3
		.amdhsa_dx10_clamp 1
		.amdhsa_ieee_mode 1
		.amdhsa_fp16_overflow 0
		.amdhsa_tg_split 0
		.amdhsa_exception_fp_ieee_invalid_op 0
		.amdhsa_exception_fp_denorm_src 0
		.amdhsa_exception_fp_ieee_div_zero 0
		.amdhsa_exception_fp_ieee_overflow 0
		.amdhsa_exception_fp_ieee_underflow 0
		.amdhsa_exception_fp_ieee_inexact 0
		.amdhsa_exception_int_div_zero 0
	.end_amdhsa_kernel

; __global__ void __launch_bounds__(NWAVES * 64, 2) fwd_kernel(Args args) {
amdhsa.kernels:
  - .agpr_count:     0
    .args:
      - .offset:         0
        .size:           272
        .value_kind:     by_value
      - .offset:         272
        .size:           4
        .value_kind:     hidden_block_count_x
      - .offset:         276
        .size:           4
        .value_kind:     hidden_block_count_y
      - .offset:         280
        .size:           4
        .value_kind:     hidden_block_count_z
      - .offset:         284
        .size:           2
        .value_kind:     hidden_group_size_x
      - .offset:         286
        .size:           2
        .value_kind:     hidden_group_size_y
      - .offset:         288
        .size:           2
        .value_kind:     hidden_group_size_z
      - .offset:         290
        .size:           2
        .value_kind:     hidden_remainder_x
      - .offset:         292
        .size:           2
        .value_kind:     hidden_remainder_y
      - .offset:         294
        .size:           2
        .value_kind:     hidden_remainder_z
      - .offset:         312
        .size:           8
        .value_kind:     hidden_global_offset_x
      - .offset:         320
        .size:           8
        .value_kind:     hidden_global_offset_y
      - .offset:         328
        .size:           8
        .value_kind:     hidden_global_offset_z
      - .offset:         336
        .size:           2
        .value_kind:     hidden_grid_dims
      - .offset:         392
        .size:           4
        .value_kind:     hidden_dynamic_lds_size
    .group_segment_fixed_size: 0
    .kernarg_segment_align: 8
    .kernarg_segment_size: 528
    .language:       OpenCL C
    .language_version:
      - 2
      - 0
    .max_flat_workgroup_size: 512
    .name:           _Z10fwd_kernel4Args
    .private_segment_fixed_size: 0
    .sgpr_count:     108
    .sgpr_spill_count: 22
    .symbol:         _Z10fwd_kernel4Args.kd
    .uniform_work_group_size: 1
    .uses_dynamic_stack: false
    .vgpr_count:     256
    .vgpr_spill_count: 0
    .wavefront_size: 64
